# conversion stores on a scalar base advanced by SALU (saddr global_store); second-half V fragment reads fold +0x2000 into the ds_read offsets
# speedup vs baseline: 1.0067x; 1.0018x over previous
; DEVI int tidx() { int t = threadIdx.x; asm volatile("" : "+v"(t)); __builtin_assume(t >= 0 && t < 512); return t; }
; DEVI unsigned cvt_pk_bf16(float lo, float hi) { unsigned r; asm volatile("v_cvt_pk_bf16_f32 %0, %1, %2" : "=v"(r) : "v"(lo), "v"(hi)); return r; }
; DEVI float bf2f(bf16_t h) { return __uint_as_float(((unsigned)h) << 16); }
; DEVI void attn_unit8(const Params& p, char* smem, int unit, int l, int& cvs  , CvRun& crun) {
;     const int tid = tidx(), wid = __builtin_amdgcn_readfirstlane(tid >> 6), lane = tid & 63, r32 = lane & 31, hi = lane >> 5;
;     const int x8 = unit & 7, v8 = unit >> 3, bh = x8 + 8 * (v8 >> 4), qt = v8 & 15, b = bh >> 3, hh = bh & 7;
;     char* K_lds = smem; char* V_lds = smem + 73728;
;     float* wsx = (float*)(smem + 122880) + wid * 64; float* li_l = wsx; float* al_l = wsx + 32;
;     const bf16_t* Kg = p.kfull + (size_t)bh * S_ * 96; const bf16_t* Vg = p.vfull + (size_t)bh * S_ * 64;
;     const size_t qtok = (size_t)b * S_ + qt * 256 + wid * 32 + r32;
;     bf16x8 qr[6];
;     { const bf16_t* qp = p.qbuf + qtok * 768 + hh * 96 + hi * 8;
; #pragma unroll
;       for (int d0 = 0; d0 < 6; ++d0) qr[d0] = *(const bf16x8*)(qp + d0 * 16);
;       const f32x4 c0 = *(const f32x4*)(p.cs + qtok * 16 + hi * 8), c1 = *(const f32x4*)(p.cs + qtok * 16 + hi * 8 + 4);
;       const f32x4 s0 = *(const f32x4*)(p.sn + qtok * 16 + hi * 8), s1 = *(const f32x4*)(p.sn + qtok * 16 + hi * 8 + 4);
;       float o1[8], o2[8];
; #pragma unroll
;       for (int j = 0; j < 8; ++j) { const float x1 = bf2f((bf16_t)qr[4][j]), x2 = bf2f((bf16_t)qr[5][j]); const float cc = j < 4 ? c0[j] : c1[j - 4], ss = j < 4 ? s0[j] : s1[j - 4];
;           o1[j] = x1 * cc - x2 * ss; o2[j] = x2 * cc + x1 * ss; }
;       u32x4 w1, w2;
; #pragma unroll
;       for (int j = 0; j < 4; ++j) { w1[j] = cvt_pk_bf16(o1[2 * j], o1[2 * j + 1]); w2[j] = cvt_pk_bf16(o2[2 * j], o2[2 * j + 1]); }
;       qr[4] = *(bf16x8*)&w1; qr[5] = *(bf16x8*)&w2; }
.LBB0_665:
	v_mov_b32_e32 v86, v0
	s_ashr_i32 s5, s83, 4
	v_readfirstlane_b32 s4, v86
	s_lshr_b32 s53, s4, 6
	s_and_b32 s52, s5, -8
	s_and_b32 s8, s4, 0x3fffffc0
	s_load_dwordx4 s[4:7], s[24:25], 0x1a0
	s_load_dwordx4 s[12:15], s[24:25], 0x110
	s_and_b32 s87, s83, 7
	s_ashr_i32 s16, s83, 7
	s_lshl_b32 s8, s8, 2
	s_or_b32 s10, s52, s87
	s_add_i32 s91, s8, 0
	s_ashr_i32 s17, s16, 31
	s_lshl_b32 s8, s83, 5
	s_ashr_i32 s11, s10, 31
	s_lshl_b64 s[16:17], s[16:17], 12
	s_and_b32 s8, s8, 0xf00
	s_and_b32 s2, s62, 7
	s_add_i32 s91, s91, 0x1e000
	s_waitcnt lgkmcnt(0)
	v_mov_b32_e32 v2, s4
	v_mov_b32_e32 v3, s5
	s_lshl_b64 s[4:5], s[10:11], 19
	s_or_b32 s8, s16, s8
	s_lshl_b32 s11, s53, 5
	v_and_b32_e32 v176, 31, v86
	s_add_u32 s48, s8, s11
	v_or_b32_e32 v10, s48, v176
	s_movk_i32 s8, 0x600
	s_addc_u32 s49, s17, 0
	v_mad_u64_u32 v[2:3], s[16:17], v10, s8, v[2:3]
	v_bfe_u32 v186, v86, 5, 1
	v_mad_i32_i24 v3, s49, v177, v3
	s_mul_i32 s8, s87, 0xc0
	v_mov_b32_e32 v11, s49
	v_lshl_add_u64 v[2:3], v[2:3], 0, s[8:9]
	v_lshlrev_b32_e32 v178, 4, v186
	v_mov_b32_e32 v179, v175
	v_lshl_add_u64 v[26:27], v[2:3], 0, v[178:179]
	v_lshlrev_b64 v[10:11], 6, v[10:11]
	global_load_dwordx4 v[2:5], v[26:27], off offset:128
	global_load_dwordx4 v[6:9], v[26:27], off offset:160
	v_lshl_add_u64 v[12:13], s[12:13], 0, v[10:11]
	v_and_b32_e32 v174, 32, v86
	v_lshl_add_u64 v[10:11], s[14:15], 0, v[10:11]
	v_lshl_add_u64 v[22:23], v[12:13], 0, v[174:175]
	v_lshl_add_u64 v[18:19], v[10:11], 0, v[174:175]
	global_load_dwordx4 v[10:13], v[18:19], off
	global_load_dwordx4 v[14:17], v[22:23], off
	s_nop 0
	global_load_dwordx4 v[18:21], v[18:19], off offset:16
	s_nop 0
	global_load_dwordx4 v[22:25], v[22:23], off offset:16
	s_load_dwordx2 s[50:51], s[24:25], 0x1b0
	global_load_dwordx4 v[150:153], v[26:27], off
	global_load_dwordx4 v[138:141], v[26:27], off offset:32
	global_load_dwordx4 v[134:137], v[26:27], off offset:64
	global_load_dwordx4 v[130:133], v[26:27], off offset:96
	s_mul_hi_i32 s8, s10, 0xc0000
	s_mul_i32 s10, s10, 0xc0000
	s_add_u32 s10, s6, s10
	s_addc_u32 s11, s7, s8
	s_lshl_b32 s61, s53, 10
	s_add_i32 s96, s61, 0
	s_waitcnt lgkmcnt(0)
	s_add_u32 s4, s50, s4
	s_mov_b32 m0, s96
	v_lshlrev_b32_e32 v88, 6, v186
	s_addc_u32 s5, s51, s5
	s_add_i32 s97, s75, s61
	v_lshlrev_b32_e32 v90, 2, v86
	v_and_b32_e32 v91, 63, v86
	v_lshlrev_b32_e32 v93, 4, v91
	v_lshlrev_b32_e32 v92, 3, v91
	v_lshlrev_b32_e32 v94, 1, v91
	s_mov_b32 s8, s9
	s_mov_b32 s12, s9
	s_mov_b32 s13, s9
	s_mov_b32 s14, s9
	s_mov_b32 s15, s9
	s_mov_b32 s16, s9
	s_mov_b32 s17, s9
	s_mov_b32 s18, s9
	s_mov_b32 s19, s9
	s_mov_b32 s20, s9
	s_mov_b32 s21, s9
	s_mov_b32 s22, s9
	s_mov_b32 s23, s9
	s_mulk_i32 s53, 0x900
	v_mov_b32_e32 v83, v175
	v_mov_b32_e32 v85, v175
	v_and_b32_e32 v114, 28, v90
	v_lshl_add_u32 v187, v176, 2, s91
	v_mul_u32_u24_e32 v201, 0x44, v114
	v_bfe_u32 v195, v91, 1, 2
	v_mov_b32_e32 v207, 1.0
	s_mov_b32 s89, s9
	v_mov_b32_e32 v188, v175
	s_waitcnt vmcnt(9)
	v_lshlrev_b32_e32 v27, 16, v2
	s_waitcnt vmcnt(8)
	v_lshlrev_b32_e32 v26, 16, v6
	v_and_b32_e32 v33, 0xffff0000, v2
	v_lshlrev_b32_e32 v35, 16, v3
	s_waitcnt vmcnt(7)
	v_mov_b32_e32 v28, v10
	s_waitcnt vmcnt(6)
	v_mov_b32_e32 v29, v14
	v_mov_b32_e32 v36, v12
	v_mov_b32_e32 v37, v16
	v_mov_b32_e32 v38, v16
	v_mov_b32_e32 v39, v12
	v_and_b32_e32 v3, 0xffff0000, v3
	v_and_b32_e32 v2, 0xffff0000, v7
	v_mov_b32_e32 v16, v13
	v_mov_b32_e32 v12, v17
	v_and_b32_e32 v32, 0xffff0000, v6
	v_lshlrev_b32_e32 v34, 16, v7
	v_pk_mul_f32 v[6:7], v[28:29], v[26:27]
	v_pk_mul_f32 v[16:17], v[16:17], v[2:3]
	v_pk_mul_f32 v[2:3], v[12:13], v[2:3]
	v_mov_b32_e32 v30, v14
	v_mov_b32_e32 v31, v10
	v_sub_f32_e32 v12, v7, v6
	v_sub_f32_e32 v16, v17, v16
	v_add_f32_e32 v17, v2, v3
	v_lshlrev_b32_e32 v3, 16, v4
	v_lshlrev_b32_e32 v2, 16, v8
	s_waitcnt vmcnt(5)
	v_mov_b32_e32 v6, v18
	s_waitcnt vmcnt(4)
	v_mov_b32_e32 v7, v22
	v_pk_mul_f32 v[26:27], v[30:31], v[26:27]
	v_pk_mul_f32 v[6:7], v[6:7], v[2:3]
	v_add_f32_e32 v13, v26, v27
	v_sub_f32_e32 v26, v7, v6
	v_mov_b32_e32 v6, v22
	v_mov_b32_e32 v7, v18
	v_pk_mul_f32 v[2:3], v[6:7], v[2:3]
	v_mov_b32_e32 v22, v19
	v_add_f32_e32 v27, v2, v3
	v_and_b32_e32 v3, 0xffff0000, v4
	v_and_b32_e32 v2, 0xffff0000, v8
	v_mov_b32_e32 v18, v23
	v_pk_mul_f32 v[6:7], v[22:23], v[2:3]
	v_pk_mul_f32 v[2:3], v[18:19], v[2:3]
	v_sub_f32_e32 v8, v7, v6
	v_add_f32_e32 v18, v2, v3
	v_lshlrev_b32_e32 v3, 16, v5
	v_lshlrev_b32_e32 v2, 16, v9
	v_mov_b32_e32 v6, v20
	v_mov_b32_e32 v7, v24
	v_pk_mul_f32 v[6:7], v[6:7], v[2:3]
	v_mov_b32_e32 v14, v11
	v_sub_f32_e32 v19, v7, v6
	v_mov_b32_e32 v6, v24
	v_mov_b32_e32 v7, v20
	v_pk_mul_f32 v[2:3], v[6:7], v[2:3]
	v_mov_b32_e32 v24, v21
	v_add_f32_e32 v6, v2, v3
	v_and_b32_e32 v3, 0xffff0000, v5
	v_and_b32_e32 v2, 0xffff0000, v9
	v_mov_b32_e32 v20, v25
	v_mov_b32_e32 v10, v15
	v_pk_mul_f32 v[4:5], v[24:25], v[2:3]
	v_pk_mul_f32 v[2:3], v[20:21], v[2:3]
	v_pk_mul_f32 v[14:15], v[14:15], v[32:33]
	v_pk_mul_f32 v[10:11], v[10:11], v[32:33]
	v_pk_mul_f32 v[28:29], v[36:37], v[34:35]
	v_pk_mul_f32 v[30:31], v[38:39], v[34:35]
	v_add_f32_e32 v2, v2, v3
	v_sub_f32_e32 v14, v15, v14
	v_add_f32_e32 v10, v10, v11
	v_sub_f32_e32 v11, v29, v28
	v_add_f32_e32 v15, v30, v31
	v_sub_f32_e32 v4, v5, v4
	v_cvt_pk_bf16_f32 v146, v12, v14
	v_cvt_pk_bf16_f32 v142, v13, v10
	v_cvt_pk_bf16_f32 v147, v11, v16
	v_cvt_pk_bf16_f32 v143, v15, v17
	v_cvt_pk_bf16_f32 v148, v26, v8
	v_cvt_pk_bf16_f32 v144, v27, v18
	v_cvt_pk_bf16_f32 v149, v19, v4
	v_cvt_pk_bf16_f32 v145, v6, v2
	v_mul_u32_u24_e32 v2, 0xaaab, v86
	v_lshrrev_b32_e32 v3, 19, v2
	v_mul_lo_u16_e32 v4, 12, v3
	v_sub_u16_e32 v4, v86, v4
	v_lshrrev_b32_e32 v2, 21, v2
; #define LAS __attribute__((address_space(3)))
; DEVI int v_rd_base(int lane) { return ((lane & 3) << 3) | (((lane >> 2) & 3) << 6) | (((lane >> 4) & 1) << 5) | (((lane >> 5) & 1) << 8); }
; #define VM0() asm volatile("s_waitcnt vmcnt(0)" ::: "memory")
; DEVI void attn_unit8(const Params& p, char* smem, int unit, int l, int& cvs  , CvRun& crun) {
;     ...
;     int ksrc[3];
; #pragma unroll
;     for (int i = 0; i < 3; ++i) { const int pc = tid + 512 * i, row = pc / 12, ch = (pc % 12) ^ ((row >> 2) & 3); ksrc[i] = row * 192 + ch * 16; }
;     const int vsrc = wid * 1024 + ((lane >> 2) & 7) * 128 + (lane >> 5) * 64 + (lane & 3) * 16;
;     LAS char* const Kl = (LAS char*)K_lds + wid * 1024; LAS char* const Vl = (LAS char*)V_lds + wid * 1024;
;     ...
;     const int vb0 = (int)(uintptr_t)(LAS char*)V_lds + v_rd_base(lane);
;     float m_reg = 0.f, l_reg = 0.f; f32x16 o[2];
; #pragma unroll
;     for (int d = 0; d < 2; ++d)
; #pragma unroll
;         for (int r = 0; r < 16; ++r) o[d][r] = 0.f;
;     f32x16 pA0, pA1, pB0, pB1; float alA, alB; bf16x8 pa0, pa1, pa2, pa3;
;     constexpr int NTILE = S_ / 128;
;     B_DMA(0, 0); B_DMA(1, 1); VM0(); __syncthreads();
	v_bitop3_b32 v2, v2, v4, 3 bitop3:0x6c
	v_mul_u32_u24_e32 v3, 0xc0, v3
	v_lshl_add_u32 v174, v2, 4, v3
	v_or_b32_e32 v2, 0x200, v86
	v_mul_u32_u24_sdwa v3, v2, s74 dst_sel:DWORD dst_unused:UNUSED_PAD src0_sel:WORD_0 src1_sel:DWORD
	v_lshrrev_b32_e32 v4, 19, v3
	v_mul_lo_u16_e32 v5, 12, v4
	v_sub_u16_e32 v2, v2, v5
	v_lshrrev_b32_e32 v3, 21, v3
	v_bitop3_b32 v2, v3, v2, 3 bitop3:0x6c
	v_mul_u32_u24_e32 v3, 0xc0, v4
	v_lshl_add_u32 v82, v2, 4, v3
	v_or_b32_e32 v2, 0x400, v86
	v_mul_u32_u24_sdwa v3, v2, s74 dst_sel:DWORD dst_unused:UNUSED_PAD src0_sel:WORD_0 src1_sel:DWORD
	v_lshrrev_b32_e32 v4, 19, v3
	v_mul_lo_u16_e32 v5, 12, v4
	v_sub_u16_e32 v2, v2, v5
	v_lshrrev_b32_e32 v3, 21, v3
	v_bitop3_b32 v2, v3, v2, 3 bitop3:0x6c
	v_mul_u32_u24_e32 v3, 0xc0, v4
	v_lshl_add_u32 v84, v2, 4, v3
	v_lshlrev_b32_e32 v2, 5, v86
	v_and_b32_e32 v87, 0x380, v2
	v_lshlrev_b32_e32 v3, 4, v86
	global_load_lds_dwordx4 v174, s[10:11]
	s_add_i32 m0, s96, 0x2000
	v_or_b32_e32 v2, v88, v87
	v_and_b32_e32 v89, 48, v3
	global_load_lds_dwordx4 v82, s[10:11]
	s_add_i32 m0, s96, 0x4000
	v_or3_b32 v2, v2, v89, s61
	global_load_lds_dwordx4 v84, s[10:11]
	v_mov_b32_e32 v3, v175
	s_mov_b32 m0, s97
	v_lshl_add_u64 v[4:5], s[4:5], 0, v[2:3]
	global_load_lds_dwordx4 v2, s[4:5]
	s_add_i32 m0, s97, 0x2000
	s_mov_b64 s[72:73], 0x2000
	v_lshl_add_u64 v[2:3], v[4:5], 0, s[72:73]
	s_add_u32 s4, s10, 0x6000
	global_load_lds_dwordx4 v[2:3], off
	s_addc_u32 s5, s11, 0
	s_add_i32 m0, s96, 0x6000
	v_lshl_add_u64 v[2:3], v[4:5], 0, s[44:45]
	global_load_lds_dwordx4 v174, s[4:5]
	s_add_i32 m0, s96, 0x8000
	v_mul_u32_u24_e32 v10, 0xc0, v176
	global_load_lds_dwordx4 v82, s[4:5]
	s_add_i32 m0, s96, 0xa000
	v_and_b32_e32 v11, 48, v90
	global_load_lds_dwordx4 v84, s[4:5]
	s_add_i32 m0, s97, 0x4000
	v_bitop3_b32 v129, v178, v10, v11 bitop3:0xde
	global_load_lds_dwordx4 v[2:3], off
	v_lshl_add_u64 v[2:3], v[4:5], 0, s[42:43]
	s_add_i32 m0, s97, 0x6000
	v_add_u32_e32 v189, 0, v129
	global_load_lds_dwordx4 v[2:3], off
	s_waitcnt vmcnt(0)
	s_waitcnt vmcnt(0) lgkmcnt(0)
	s_barrier
; #define VM0() asm volatile("s_waitcnt vmcnt(0)" ::: "memory")
; #define C_SPLAT() do { _Pragma("unroll") for (int _r = 0; _r < 16; ++_r) cinit[_r] = -m_reg; asm volatile("" : "+v"(cinit)); } while (0)
; template <bool FIRST> DEVI bool partialSM(f32x16& p0, f32x16& p1, float& m_reg, float& alpha) {
;     float pmax = p0[0];
; #pragma unroll
;     for (int r = 1; r < 16; ++r) pmax = fmaxf(pmax, p0[r]);
; #pragma unroll
;     for (int r = 0; r < 16; ++r) pmax = fmaxf(pmax, p1[r]);
;     { auto rr = __builtin_amdgcn_permlane32_swap(__float_as_uint(pmax), __float_as_uint(pmax), false, false);
;       pmax = fmaxf(__uint_as_float(rr[0]), __uint_as_float(rr[1])); }
;     if (FIRST) { m_reg = pmax; alpha = 1.f;
; #pragma unroll
;         for (int r = 0; r < 16; ++r) { p0[r] = __builtin_amdgcn_exp2f(p0[r] - pmax); p1[r] = p1[r] - pmax; }
;         return false;
; DEVI void attn_unit8(const Params& p, char* smem, int unit, int l, int& cvs  , CvRun& crun) {
;     ...
;     float m_reg = 0.f, l_reg = 0.f; f32x16 o[2];
; #pragma unroll
;     for (int d = 0; d < 2; ++d)
; #pragma unroll
;         for (int r = 0; r < 16; ++r) o[d][r] = 0.f;
;     f32x16 pA0, pA1, pB0, pB1; float alA, alB; bf16x8 pa0, pa1, pa2, pa3;
;     constexpr int NTILE = S_ / 128;
;     B_DMA(0, 0); B_DMA(1, 1); VM0(); __syncthreads();
;     f32x16 cinit;
;     ...
;     { f32x16 z; _Pragma("unroll") for (int r = 0; r < 16; ++r) z[r] = 0.f;
;       qkt(pA0, pA1, K_lds, qr, r32, hi, z); } partialSM<true>(pA0, pA1, m_reg, alA); C_SPLAT();
;     int s0 = 0, s1 = 1, s2 = 2;
	ds_read_b128 v[2:5], v189
	ds_read_b128 v[6:9], v189 offset:6144
	s_waitcnt lgkmcnt(1)
	v_mfma_f32_32x32x16_bf16 v[34:49], v[2:5], v[150:153], 0
	v_or_b32_e32 v2, 32, v178
	v_bitop3_b32 v184, v2, v10, v11 bitop3:0xde
	v_add_u32_e32 v190, 0, v184
	s_mov_b32 s10, s9
	s_mov_b32 s11, s9
	s_lshl_b32 s71, s54, 5
	s_lshl_b32 s84, s54, 4
	s_waitcnt lgkmcnt(0)
	v_mfma_f32_32x32x16_bf16 v[18:33], v[6:9], v[150:153], 0
	ds_read_b128 v[2:5], v190
	ds_read_b128 v[6:9], v190 offset:6144
	s_lshl_b32 s85, s54, 3
	s_lshl_b32 s88, s54, 1
	v_cmp_gt_u32_e64 s[4:5], 32, v91
	s_waitcnt lgkmcnt(1)
	v_mfma_f32_32x32x16_bf16 v[34:49], v[2:5], v[138:141], v[34:49]
	v_or_b32_e32 v2, 64, v178
	v_xad_u32 v185, v2, v11, v10
	v_add_u32_e32 v191, 0, v185
	s_waitcnt lgkmcnt(0)
	v_mfma_f32_32x32x16_bf16 v[18:33], v[6:9], v[138:141], v[18:33]
	ds_read_b128 v[2:5], v191
	ds_read_b128 v[6:9], v191 offset:6144
	s_waitcnt lgkmcnt(1)
	v_mfma_f32_32x32x16_bf16 v[34:49], v[2:5], v[134:137], v[34:49]
	v_or_b32_e32 v2, 0x60, v178
	v_xad_u32 v204, v2, v11, v10
	v_add_u32_e32 v192, 0, v204
	ds_read_b128 v[2:5], v192
	s_waitcnt lgkmcnt(1)
	v_mfma_f32_32x32x16_bf16 v[18:33], v[6:9], v[134:137], v[18:33]
	ds_read_b128 v[6:9], v192 offset:6144
	s_waitcnt lgkmcnt(1)
	v_mfma_f32_32x32x16_bf16 v[34:49], v[2:5], v[130:133], v[34:49]
	v_and_b32_e32 v2, 0xc0, v93
	v_and_or_b32 v12, v92, 24, v2
	v_or_b32_e32 v2, 0x80, v178
	v_xad_u32 v205, v2, v11, v10
	v_add_u32_e32 v193, 0, v205
	ds_read_b128 v[2:5], v193
	s_waitcnt lgkmcnt(1)
	v_mfma_f32_32x32x16_bf16 v[18:33], v[6:9], v[130:133], v[18:33]
	v_and_b32_e32 v6, 32, v94
	v_and_b32_e32 v7, 0x100, v92
	v_or3_b32 v179, v12, v6, v7
	ds_read_b128 v[6:9], v193 offset:6144
	v_add_u32_e32 v115, s75, v179
	s_waitcnt lgkmcnt(1)
	v_mfma_f32_32x32x16_bf16 v[34:49], v[2:5], v[146:149], v[34:49]
	v_or_b32_e32 v2, 0xa0, v178
	v_xad_u32 v206, v2, v11, v10
	v_add_u32_e32 v194, 0, v206
	ds_read_b128 v[2:5], v194
	ds_read_b128 v[50:53], v194 offset:6144
	s_waitcnt lgkmcnt(2)
	v_mfma_f32_32x32x16_bf16 v[18:33], v[6:9], v[146:149], v[18:33]
	s_waitcnt lgkmcnt(1)
	v_mfma_f32_32x32x16_bf16 v[34:49], v[2:5], v[142:145], v[34:49]
	v_mov_b64_e32 v[2:3], s[8:9]
	v_mov_b64_e32 v[4:5], s[10:11]
	v_mov_b64_e32 v[6:7], s[12:13]
	v_mov_b64_e32 v[8:9], s[14:15]
	v_mov_b64_e32 v[10:11], s[16:17]
	v_mov_b64_e32 v[12:13], s[18:19]
	v_mov_b64_e32 v[14:15], s[20:21]
	s_waitcnt lgkmcnt(0)
	v_mfma_f32_32x32x16_bf16 v[18:33], v[50:53], v[142:145], v[18:33]
	s_nop 2
	v_max_f32_e32 v50, v35, v35
	v_max_f32_e32 v51, v34, v34
	v_max_f32_e32 v50, v51, v50
	v_max3_f32 v50, v50, v36, v37
	v_max3_f32 v50, v50, v38, v39
	v_max3_f32 v50, v50, v40, v41
	v_max3_f32 v50, v50, v42, v43
	v_max3_f32 v50, v50, v44, v45
	v_max3_f32 v50, v50, v46, v47
	v_max3_f32 v50, v50, v48, v49
	v_max3_f32 v50, v50, v18, v19
	v_max3_f32 v50, v50, v20, v21
	v_max3_f32 v50, v50, v22, v23
	v_max3_f32 v50, v50, v24, v25
	v_max3_f32 v50, v50, v26, v27
	v_max3_f32 v50, v50, v28, v29
	v_max3_f32 v50, v50, v30, v31
	v_max3_f32 v50, v50, v32, v33
	v_mov_b32_e32 v51, v50
	s_nop 1
	v_permlane32_swap_b32_e32 v50, v51
	v_max_f32_e32 v51, v51, v51
	v_max_f32_e32 v50, v50, v50
	v_max_f32_e32 v203, v50, v51
	v_sub_f32_e32 v34, v34, v203
	v_exp_f32_e32 v50, v34
	v_sub_f32_e32 v34, v35, v203
	v_exp_f32_e32 v51, v34
	v_sub_f32_e32 v34, v36, v203
	v_exp_f32_e32 v52, v34
	v_sub_f32_e32 v34, v37, v203
	v_exp_f32_e32 v53, v34
	v_sub_f32_e32 v34, v38, v203
	v_exp_f32_e32 v54, v34
	v_sub_f32_e32 v34, v39, v203
	v_exp_f32_e32 v55, v34
	v_sub_f32_e32 v34, v40, v203
	v_exp_f32_e32 v56, v34
	v_sub_f32_e32 v34, v41, v203
	v_exp_f32_e32 v57, v34
	v_sub_f32_e32 v34, v42, v203
	v_mov_b64_e32 v[16:17], s[22:23]
	v_exp_f32_e32 v58, v34
	v_sub_f32_e32 v34, v43, v203
	v_sub_f32_e32 v67, v19, v203
	s_add_i32 s8, s53, 0
	v_bfe_u32 v19, v86, 1, 5
	v_exp_f32_e32 v59, v34
	v_sub_f32_e32 v34, v44, v203
	v_sub_f32_e32 v68, v20, v203
	s_add_i32 s8, s8, 0x1e800
	v_and_b32_e32 v20, 28, v19
	s_or_b32 s10, s52, s2
	v_exp_f32_e32 v60, v34
	v_sub_f32_e32 v34, v45, v203
	v_sub_f32_e32 v69, v21, v203
	v_add_u32_e32 v200, s8, v20
	v_mov_b32_e32 v21, s8
	s_lshl_b32 s8, s54, 10
	s_ashr_i32 s11, s10, 31
	v_exp_f32_e32 v61, v34
	v_sub_f32_e32 v34, v46, v203
	s_add_i32 s70, s8, 0xf7f80000
	s_lshl_b64 s[12:13], s[10:11], 19
	v_exp_f32_e32 v62, v34
	v_sub_f32_e32 v34, v47, v203
	v_sub_f32_e32 v66, v18, v203
	v_lshrrev_b32_e32 v18, 2, v86
	s_add_u32 s12, s50, s12
	v_exp_f32_e32 v63, v34
	v_sub_f32_e32 v34, v48, v203
	v_sub_f32_e32 v70, v22, v203
	v_and_b32_e32 v128, 14, v18
	v_lshrrev_b32_e32 v22, 3, v86
	v_and_b32_e32 v18, 12, v18
	s_addc_u32 s13, s51, s13
	s_mul_i32 s8, s10, 0xc0000
	v_exp_f32_e32 v64, v34
	v_sub_f32_e32 v34, v49, v203
	v_mad_u32_u24 v198, v19, s77, v21
	v_and_b32_e32 v19, 0x80, v92
	v_and_b32_e32 v21, 16, v94
	v_and_b32_e32 v22, 4, v22
	v_and_or_b32 v197, v93, s76, v18
	v_or_b32_e32 v18, s61, v87
	s_mul_hi_i32 s2, s10, 0xc0000
	s_add_u32 s6, s6, s8
	v_exp_f32_e32 v65, v34
	v_or3_b32 v196, v19, v22, v21
	v_or3_b32 v18, v18, v88, v89
	v_mov_b32_e32 v19, v175
	s_addc_u32 s2, s7, s2
	v_and_b32_e32 v20, 1, v86

; #define LAS __attribute__((address_space(3)))
; DEVI int v_rd_base(int lane) { return ((lane & 3) << 3) | (((lane >> 2) & 3) << 6) | (((lane >> 4) & 1) << 5) | (((lane >> 5) & 1) << 8); }
; #define VM0() asm volatile("s_waitcnt vmcnt(0)" ::: "memory")
; #define C_SPLAT() do { _Pragma("unroll") for (int _r = 0; _r < 16; ++_r) cinit[_r] = -m_reg; asm volatile("" : "+v"(cinit)); } while (0)
; DEVI void attn_unit8(const Params& p, char* smem, int unit, int l, int& cvs  , CvRun& crun) {
;     ...
;     const int vsrc = wid * 1024 + ((lane >> 2) & 7) * 128 + (lane >> 5) * 64 + (lane & 3) * 16;
;     LAS char* const Kl = (LAS char*)K_lds + wid * 1024; LAS char* const Vl = (LAS char*)V_lds + wid * 1024;
;     ...
;     const int vb0 = (int)(uintptr_t)(LAS char*)V_lds + v_rd_base(lane);
;     float m_reg = 0.f, l_reg = 0.f; f32x16 o[2];
; #pragma unroll
;     for (int d = 0; d < 2; ++d)
; #pragma unroll
;         for (int r = 0; r < 16; ++r) o[d][r] = 0.f;
;     f32x16 pA0, pA1, pB0, pB1; float alA, alB; bf16x8 pa0, pa1, pa2, pa3;
;     constexpr int NTILE = S_ / 128;
;     B_DMA(0, 0); B_DMA(1, 1); VM0(); __syncthreads();
;     f32x16 cinit;
;     ...
;     { f32x16 z; _Pragma("unroll") for (int r = 0; r < 16; ++r) z[r] = 0.f;
;       qkt(pA0, pA1, K_lds, qr, r32, hi, z); } partialSM<true>(pA0, pA1, m_reg, alA); C_SPLAT();
;     int s0 = 0, s1 = 1, s2 = 2;
	s_add_u32 s6, s6, 0xc000
	v_xor_b32_e32 v34, 0x80000000, v203
	v_sub_f32_e32 v81, v33, v203
	v_sub_f32_e32 v80, v32, v203
	v_sub_f32_e32 v79, v31, v203
	v_sub_f32_e32 v78, v30, v203
	v_sub_f32_e32 v77, v29, v203
	v_sub_f32_e32 v76, v28, v203
	v_sub_f32_e32 v75, v27, v203
	v_sub_f32_e32 v74, v26, v203
	v_sub_f32_e32 v73, v25, v203
	v_sub_f32_e32 v72, v24, v203
	v_sub_f32_e32 v71, v23, v203
	v_lshlrev_b32_e32 v199, 5, v20
	v_lshlrev_b32_e32 v180, 4, v20
	v_mov_b32_e32 v116, v18
	v_add_u32_e32 v117, 0x2000, v18
	s_addc_u32 s7, s2, 0
	s_add_u32 s44, s12, 0x8000
	s_addc_u32 s45, s13, 0
	v_mov_b64_e32 v[32:33], v[16:17]
	v_mov_b32_e32 v35, v34
	v_mov_b32_e32 v36, v34
	v_mov_b32_e32 v37, v34
	v_mov_b32_e32 v38, v34
	v_mov_b32_e32 v39, v34
	v_mov_b32_e32 v40, v34
	v_mov_b32_e32 v41, v34
	v_mov_b32_e32 v42, v34
	v_mov_b32_e32 v43, v34
	v_mov_b32_e32 v44, v34
	v_mov_b32_e32 v45, v34
	v_mov_b32_e32 v46, v34
	v_mov_b32_e32 v47, v34
	v_mov_b32_e32 v48, v34
	v_mov_b32_e32 v49, v34
	v_mov_b32_e32 v118, v174
	v_mov_b32_e32 v120, v82
	v_mov_b32_e32 v122, v84
	s_mov_b64 s[12:13], s[6:7]
	s_add_u32 s67, s6, 0xb4000
	v_mov_b64_e32 v[30:31], v[14:15]
	v_mov_b64_e32 v[28:29], v[12:13]
	v_mov_b64_e32 v[26:27], v[10:11]
	v_mov_b64_e32 v[24:25], v[8:9]
	v_mov_b64_e32 v[22:23], v[6:7]
	v_mov_b64_e32 v[20:21], v[4:5]
	v_mov_b64_e32 v[18:19], v[2:3]
	s_mov_b32 s6, 2
	s_mov_b32 s2, 1

; DEVI f32x4 ld_nt(const float* p) { return __builtin_nontemporal_load((const f32x4*)p); }
; DEVI void cv_next(const Params& p, int l, int s, int lane, int stride, CvRun& run) {
;     ...
;     run.c = cv_slice(p, l, s, lane); run.left = 0;
;     if ((stride & 511) == 0) {
;         if (s < NS_W13) { const int e = s >> 9, es = stride >> 9; if (e < NE) { run.left = (NE - 1 - e) / es; run.sstep = (long)es * 1024 * 256; run.dstep = (long)es * 512 * 1024; } }
;         else { const int e = (s - NS_W13) >> 8, es = stride >> 8; if (e < NE) { run.left = (NE - 1 - e) / es; run.sstep = (long)es * 256 * 1024; run.dstep = (long)es * 1024 * 256; } } }
; }
; DEVI void cv_issue(const Params& p, int l, int s, int lane, CvRegs& R, CvRun& run) {
;     R.live = s < NS_SLICES ? 1 : 0;
;     if (R.live) { cv_next(p, l, s, lane, (int)gridDim.x * 8, run); R.c = run.c; const int kq = lane >> 3;
;         const float* sp = R.c.src + (size_t)(R.c.k0 + 2 * kq) * R.c.ld;
;         R.a0 = ld_nt(sp); R.b0 = ld_nt(sp + R.c.ld); R.a1 = ld_nt(sp + (size_t)16 * R.c.ld); R.b1 = ld_nt(sp + (size_t)17 * R.c.ld); }
.LBB0_693:
	s_and_b64 vcc, exec, s[16:17]
	s_cbranch_vccz .LBB0_695
	s_lshl_b64 s[6:7], s[26:27], 1
	s_lshl_b64 s[16:17], s[28:29], 2
	s_add_u32 s68, s68, s16
	s_addc_u32 s69, s69, s17
	s_add_u32 s40, s40, s6
	s_addc_u32 s41, s41, s7
	s_add_i32 s56, s56, -1
	s_mov_b32 s8, s60
	s_mov_b32 s94, s59
	s_mov_b32 s10, s58
	s_mov_b32 s95, s55
	s_mov_b32 s6, s57
	global_load_dwordx4 v[154:157], v242, s[68:69] nt
	global_load_dwordx4 v[158:161], v243, s[68:69] nt
	global_load_dwordx4 v[162:165], v244, s[68:69] nt
	global_load_dwordx4 v[166:169], v245, s[68:69] nt
	s_branch .LBB0_696


; DEVI f32x4 ld_nt(const float* p) { return __builtin_nontemporal_load((const f32x4*)p); }
; DEVI void cv_next(const Params& p, int l, int s, int lane, int stride, CvRun& run) {
;     ...
;     run.c = cv_slice(p, l, s, lane); run.left = 0;
;     if ((stride & 511) == 0) {
;         if (s < NS_W13) { const int e = s >> 9, es = stride >> 9; if (e < NE) { run.left = (NE - 1 - e) / es; run.sstep = (long)es * 1024 * 256; run.dstep = (long)es * 512 * 1024; } }
;         else { const int e = (s - NS_W13) >> 8, es = stride >> 8; if (e < NE) { run.left = (NE - 1 - e) / es; run.sstep = (long)es * 256 * 1024; run.dstep = (long)es * 1024 * 256; } } }
; }
; DEVI void cv_issue(const Params& p, int l, int s, int lane, CvRegs& R, CvRun& run) {
;     R.live = s < NS_SLICES ? 1 : 0;
;     if (R.live) { cv_next(p, l, s, lane, (int)gridDim.x * 8, run); R.c = run.c; const int kq = lane >> 3;
;         const float* sp = R.c.src + (size_t)(R.c.k0 + 2 * kq) * R.c.ld;
;         R.a0 = ld_nt(sp); R.b0 = ld_nt(sp + R.c.ld); R.a1 = ld_nt(sp + (size_t)16 * R.c.ld); R.b1 = ld_nt(sp + (size_t)17 * R.c.ld); }
; DEVI void cv_finish(char* img  , int lane, const CvRegs& R) {
;     ...
;     const int row = R.c.perm ? R.c.r0 + 128 * ((n >> 3) & 1) + 16 * ((n >> 2) & 1) + 4 * (n >> 4) + (n & 3) : R.c.r0 + 128 * ((n >> 2) & 1) + 4 * (n >> 3) + (n & 3);
;     bf16_t* d = R.c.dst + (size_t)row * R.c.K + R.c.k0 + half * 16;
.LBB0_695:
	v_add_u32_e32 v252, s10, v128
	s_mov_b64 s[68:69], s[18:19]
	s_mov_b64 s[40:41], s[20:21]
	v_mul_lo_u32 v243, v252, s6
	v_lshlrev_b32_e32 v242, 2, v114
	s_lshl_b32 s72, s6, 2
	s_lshl_b32 s73, s6, 6
	v_lshl_add_u32 v242, v243, 2, v242
	v_add_u32_e32 v243, s72, v242
	v_add_u32_e32 v244, s73, v242
	v_add_u32_e32 v245, s73, v243
	s_cmp_eq_u32 s95, 0
	s_cselect_b64 s[72:73], -1, 0
	v_cndmask_b32_e64 v246, v196, v197, s[72:73]
	v_or_b32_e32 v246, v246, v195
	v_add_u32_e32 v246, s8, v246
	v_mul_lo_u32 v246, v246, s94
	v_add3_u32 v246, v246, v180, s10
	v_lshlrev_b32_e32 v246, 1, v246
	v_mov_b32_e32 v247, 0
	s_ashr_i32 s7, s6, 31
	v_mad_i64_i32 v[252:253], s[16:17], v252, s6, 0
	v_lshl_add_u64 v[252:253], v[252:253], 2, v[250:251]
	s_lshl_b64 s[16:17], s[6:7], 2
	v_lshl_add_u64 v[254:255], v[252:253], 0, s[16:17]
	global_load_dwordx4 v[154:157], v[252:253], off nt
	global_load_dwordx4 v[158:161], v[254:255], off nt
	v_mad_i64_i32 v[252:253], s[18:19], s6, 60, v[254:255]
	v_lshl_add_u64 v[254:255], v[252:253], 0, s[16:17]
	global_load_dwordx4 v[162:165], v[252:253], off nt
	global_load_dwordx4 v[166:169], v[254:255], off nt
	s_mov_b64 s[26:27], s[22:23]
	s_mov_b64 s[28:29], s[50:51]
	s_mov_b32 s56, s11
	s_mov_b32 s55, s95
	v_mov_b64_e32 v[170:171], v[250:251]
	s_mov_b32 s57, s6
	s_mov_b32 s58, s10
	v_mov_b64_e32 v[172:173], v[182:183]
	s_mov_b32 s59, s94
	s_mov_b32 s60, s8

; #define VM0() asm volatile("s_waitcnt vmcnt(0)" ::: "memory")
; #define B_RESC(a, rare) do { if (rare) { if (hi == 0) al_l[r32] = (a); asm volatile("s_waitcnt lgkmcnt(0)" ::: "memory"); __builtin_amdgcn_wave_barrier(); \
;         _Pragma("unroll") for (int _d = 0; _d < 2; ++_d) _Pragma("unroll") for (int _r = 0; _r < 16; ++_r) o[_d][_r] *= al_l[crow(_r, hi)]; C_SPLAT(); } } while (0)
; DEVI void attn_unit8(const Params& p, char* smem, int unit, int l, int& cvs  , CvRun& crun) {
;     ...
;     for (int T = 0; T + 1 < NTILE; ++T) {
;         const char* Kb = K_lds + s0 * 24576; const int vb = vb0 + s0 * 16384;
;         CvRegs cvr; cv_issue(p, l, cvs, lane, cvr, crun); cvs += (int)gridDim.x * 8;
;         qkt(pB0, pB1, Kb + 12288, qr, r32, hi, cinit);
;         finishSM(pA0, pA1, alA, l_reg, pa0, pa1, pa2, pa3);
;         pv_both(o[0], o[1], vb, pa0, pa1, pa2, pa3);
;         { const bool rr_ = partialSM<false>(pB0, pB1, m_reg, alB); B_RESC(alB, rr_); }
;         cv_finish(smem + 124928 + wid * 2304, lane, cvr);
;         if (cvr.live) asm volatile("s_waitcnt vmcnt(2)" ::: "memory"); else VM0();
;         __syncthreads();
;         if (T + 2 < NTILE) B_DMA(T + 2, s2);
.LBB0_702:
	s_mul_i32 s98, s2, 0x6000
	s_add_i32 s98, s96, s98
	s_lshl_b32 s99, s2, 14
	s_add_i32 s99, s97, s99
	s_mul_i32 s6, s61, 0x6000
	s_add_i32 s6, s6, 0
	v_add_u32_e32 v249, s6, v129

; #define VM0() asm volatile("s_waitcnt vmcnt(0)" ::: "memory")
; DEVI void attn_unit8(const Params& p, char* smem, int unit, int l, int& cvs  , CvRun& crun) {
;     ...
;         if (cvr.live) asm volatile("s_waitcnt vmcnt(2)" ::: "memory"); else VM0();
;         __syncthreads();
;         if (T + 2 < NTILE) B_DMA(T + 2, s2);
;         qkt(pA0, pA1, K_lds + s1 * 24576, qr, r32, hi, cinit);
	s_mov_b32 m0, s98
	s_barrier
	ds_read_b128 v[234:237], v249
	ds_read_b128 v[210:213], v249 offset:6144
	global_load_lds_dwordx4 v118, s[12:13]
	s_waitcnt lgkmcnt(1)
	v_mfma_f32_32x32x16_bf16 v[98:113], v[234:237], v[150:153], v[34:49]
	s_add_i32 m0, s98, 0x2000

; DEVI void qkt(f32x16& p0, f32x16& p1, const char* Kb, const bf16x8 (&qr)[6], int r32, int hi, const f32x16& cinit) {
; #pragma unroll
;     for (int d0 = 0; d0 < 6; ++d0) { const int cb = (d0 * 16 + hi * 8) * 2;
;         const bf16x8 k0 = *(const bf16x8*)(Kb + KSWZ(r32, cb)), k1 = *(const bf16x8*)(Kb + KSWZ(32 + r32, cb));
;         p0 = __builtin_amdgcn_mfma_f32_32x32x16_bf16(k0, qr[d0], d0 == 0 ? cinit : p0, 0, 0, 0);
;         p1 = __builtin_amdgcn_mfma_f32_32x32x16_bf16(k1, qr[d0], d0 == 0 ? cinit : p1, 0, 0, 0); }
; }
	v_add_u32_e32 v126, s6, v184
	global_load_lds_dwordx4 v120, s[12:13]
	s_waitcnt lgkmcnt(0)
	v_mfma_f32_32x32x16_bf16 v[66:81], v[210:213], v[150:153], v[34:49]
	ds_read_b128 v[210:213], v126
	ds_read_b128 v[214:217], v126 offset:6144
	s_add_i32 m0, s98, 0x4000

; DEVI void qkt(f32x16& p0, f32x16& p1, const char* Kb, const bf16x8 (&qr)[6], int r32, int hi, const f32x16& cinit) {
; #pragma unroll
;     for (int d0 = 0; d0 < 6; ++d0) { const int cb = (d0 * 16 + hi * 8) * 2;
;         const bf16x8 k0 = *(const bf16x8*)(Kb + KSWZ(r32, cb)), k1 = *(const bf16x8*)(Kb + KSWZ(32 + r32, cb));
;         p0 = __builtin_amdgcn_mfma_f32_32x32x16_bf16(k0, qr[d0], d0 == 0 ? cinit : p0, 0, 0, 0);
;         p1 = __builtin_amdgcn_mfma_f32_32x32x16_bf16(k1, qr[d0], d0 == 0 ? cinit : p1, 0, 0, 0); }
; }
	v_add_u32_e32 v126, s6, v185
	global_load_lds_dwordx4 v122, s[12:13]
	s_waitcnt lgkmcnt(1)
	v_mfma_f32_32x32x16_bf16 v[98:113], v[210:213], v[138:141], v[98:113]
	s_mov_b32 m0, s99
	s_nop 0
	global_load_lds_dwordx4 v116, s[44:45]
	s_add_i32 m0, s99, 0x2000


; template <int OFF> DEVI s16x4 tr_read(int vb) { s16x4 r; asm volatile("ds_read_b64_tr_b16 %0, %1 offset:%2" : "=&v"(r) : "v"(vb), "i"(OFF) : "memory"); return r; }
; #define SBAR() __builtin_amdgcn_sched_barrier(0)
; #define PK4(P, BASE, OUT) do { u32x4 w = {cvt_pk_bf16(P[BASE + 0], P[BASE + 1]), cvt_pk_bf16(P[BASE + 2], P[BASE + 3]), cvt_pk_bf16(P[BASE + 4], P[BASE + 5]), cvt_pk_bf16(P[BASE + 6], P[BASE + 7])}; \
;     OUT = *reinterpret_cast<bf16x8*>(&w); } while (0)
; DEVI void pv_both(f32x16& o0, f32x16& o1, int vb, bf16x8 pa0, bf16x8 pa1, bf16x8 pa2, bf16x8 pa3) {
;     const s16x4 a0 = tr_read<v_rd_off(0, 0, 0)>(vb), b0 = tr_read<v_rd_off(0, 0, 1)>(vb), a1 = tr_read<v_rd_off(0, 1, 0)>(vb), b1 = tr_read<v_rd_off(0, 1, 1)>(vb);
;     const s16x4 a2 = tr_read<v_rd_off(0, 2, 0)>(vb), b2 = tr_read<v_rd_off(0, 2, 1)>(vb), a3 = tr_read<v_rd_off(0, 3, 0)>(vb), b3 = tr_read<v_rd_off(0, 3, 1)>(vb);
;     const s16x4 c0 = tr_read<v_rd_off(1, 0, 0)>(vb), d0 = tr_read<v_rd_off(1, 0, 1)>(vb), c1 = tr_read<v_rd_off(1, 1, 0)>(vb), d1 = tr_read<v_rd_off(1, 1, 1)>(vb);
;     const s16x4 c2 = tr_read<v_rd_off(1, 2, 0)>(vb), d2 = tr_read<v_rd_off(1, 2, 1)>(vb), c3 = tr_read<v_rd_off(1, 3, 0)>(vb), d3 = tr_read<v_rd_off(1, 3, 1)>(vb);
;     asm volatile("s_waitcnt lgkmcnt(8)" ::: "memory"); SBAR();
; DEVI void finishSM(f32x16& p0, f32x16& p1, float alpha, float& l_reg, bf16x8& pa0, bf16x8& pa1, bf16x8& pa2, bf16x8& pa3) {
; #pragma unroll
;     for (int r = 0; r < 16; ++r) p1[r] = __builtin_amdgcn_exp2f(p1[r]);
;     f32x2 s2 = (f32x2){p0[0], p0[1]} + (f32x2){p1[0], p1[1]};
; #pragma unroll
;     for (int r = 2; r < 16; r += 2) s2 += (f32x2){p0[r], p0[r + 1]} + (f32x2){p1[r], p1[r + 1]};
;     float ps = s2[0] + s2[1];
;     { auto rr = __builtin_amdgcn_permlane32_swap(__float_as_uint(ps), __float_as_uint(ps), false, false);
;       ps = __uint_as_float(rr[0]) + __uint_as_float(rr[1]); }
;     l_reg = l_reg * alpha + ps;
;     ...
;     PK4(p0, 0, pa0); PK4(p0, 8, pa1); PK4(p1, 0, pa2); PK4(p1, 8, pa3);
;     ...
; }
	s_waitcnt lgkmcnt(0)
	v_mfma_f32_32x32x16_bf16 v[66:81], v[214:217], v[138:141], v[66:81]
	global_load_lds_dwordx4 v117, s[44:45]
	ds_read_b128 v[210:213], v126
	ds_read_b128 v[214:217], v126 offset:6144
	v_add_u32_e32 v126, s6, v204
	s_waitcnt lgkmcnt(1)
	v_mfma_f32_32x32x16_bf16 v[98:113], v[210:213], v[134:137], v[98:113]
	ds_read_b128 v[210:213], v126
	ds_read_b128 v[218:221], v126 offset:6144
	v_add_u32_e32 v126, s6, v205
	s_waitcnt lgkmcnt(2)
	v_mfma_f32_32x32x16_bf16 v[66:81], v[214:217], v[134:137], v[66:81]
	ds_read_b128 v[214:217], v126
	ds_read_b128 v[222:225], v126 offset:6144
	v_add_u32_e32 v126, s6, v206
	ds_read_b128 v[226:229], v126
	ds_read_b128 v[230:233], v126 offset:6144
	v_add_f32_e32 v126, v50, v82
	v_add_f32_e32 v127, v51, v83
	v_cvt_pk_bf16_f32 v50, v50, v51
	v_cvt_pk_bf16_f32 v51, v52, v53
	s_waitcnt lgkmcnt(5)
	v_mfma_f32_32x32x16_bf16 v[98:113], v[210:213], v[130:133], v[98:113]
	v_add_f32_e64 v210, v52, v84
	v_add_f32_e64 v211, v53, v85
	v_cvt_pk_bf16_f32 v52, v54, v55
	v_cvt_pk_bf16_f32 v53, v56, v57
	v_add_f32_e64 v126, v210, v126
	v_add_f32_e64 v127, v211, v127
	v_add_f32_e64 v210, v54, v86
	v_add_f32_e64 v211, v55, v87
	v_cvt_pk_bf16_f32 v54, v58, v59
	s_waitcnt lgkmcnt(4)
	v_mfma_f32_32x32x16_bf16 v[66:81], v[218:221], v[130:133], v[66:81]
	v_add_f32_e64 v126, v210, v126
	v_add_f32_e64 v127, v211, v127
	v_add_f32_e64 v210, v56, v88
	v_add_f32_e64 v211, v57, v89
	v_cvt_pk_bf16_f32 v55, v60, v61
	v_cvt_pk_bf16_f32 v56, v62, v63
	v_cvt_pk_bf16_f32 v57, v64, v65
	v_add_f32_e64 v126, v210, v126
	v_add_f32_e64 v127, v211, v127
	v_add_f32_e32 v210, v58, v90
	v_add_f32_e32 v211, v59, v91
	v_cvt_pk_bf16_f32 v58, v82, v83
	v_cvt_pk_bf16_f32 v59, v84, v85
	s_waitcnt lgkmcnt(3)
	v_mfma_f32_32x32x16_bf16 v[98:113], v[214:217], v[146:149], v[98:113]
	v_add_f32_e64 v126, v210, v126
	v_add_f32_e64 v127, v211, v127
	v_add_f32_e64 v210, v60, v92
	v_add_f32_e64 v211, v61, v93
	v_cvt_pk_bf16_f32 v60, v86, v87
	v_cvt_pk_bf16_f32 v61, v88, v89
	v_add_f32_e64 v126, v210, v126
	v_add_f32_e64 v127, v211, v127
	v_add_f32_e32 v210, v62, v94
	v_add_f32_e32 v211, v63, v95
	v_cvt_pk_bf16_f32 v62, v90, v91
	v_cvt_pk_bf16_f32 v63, v92, v93
	s_waitcnt lgkmcnt(2)
	v_mfma_f32_32x32x16_bf16 v[66:81], v[222:225], v[146:149], v[66:81]
	v_add_f32_e64 v126, v210, v126
	v_add_f32_e64 v127, v211, v127
	v_add_f32_e64 v210, v64, v96
	v_add_f32_e64 v211, v65, v97
	v_cvt_pk_bf16_f32 v64, v94, v95
	v_cvt_pk_bf16_f32 v65, v96, v97
	ds_read_b64_tr_b16 v[154:155], v202 offset:0x2000
	ds_read_b64_tr_b16 v[156:157], v202 offset:0x2400
	ds_read_b64_tr_b16 v[158:159], v202 offset:0x2800
	ds_read_b64_tr_b16 v[160:161], v202 offset:0x2c00
	ds_read_b64_tr_b16 v[162:163], v202 offset:0x3000
	ds_read_b64_tr_b16 v[164:165], v202 offset:0x3400
	ds_read_b64_tr_b16 v[166:167], v202 offset:0x3800
	ds_read_b64_tr_b16 v[168:169], v202 offset:0x3c00
	v_add_f32_e64 v126, v210, v126
	v_add_f32_e64 v127, v211, v127
	ds_read_b64_tr_b16 v[210:211], v202 offset:0x2200
	ds_read_b64_tr_b16 v[212:213], v202 offset:0x2600
	ds_read_b64_tr_b16 v[214:215], v202 offset:0x2a00
	s_waitcnt lgkmcnt(12)
	v_mfma_f32_32x32x16_bf16 v[98:113], v[226:229], v[142:145], v[98:113]
	ds_read_b64_tr_b16 v[216:217], v202 offset:0x2e00
	ds_read_b64_tr_b16 v[218:219], v202 offset:0x3200
	ds_read_b64_tr_b16 v[220:221], v202 offset:0x3600
	ds_read_b64_tr_b16 v[222:223], v202 offset:0x3a00
	ds_read_b64_tr_b16 v[224:225], v202 offset:0x3e00
	v_add_f32_e32 v126, v126, v127
	s_waitcnt lgkmcnt(15)
	v_mfma_f32_32x32x16_bf16 v[66:81], v[230:233], v[142:145], v[66:81]
	v_mov_b32_e32 v127, v126


; #define SBAR() __builtin_amdgcn_sched_barrier(0)
; DEVI void pv_both(f32x16& o0, f32x16& o1, int vb, bf16x8 pa0, bf16x8 pa1, bf16x8 pa2, bf16x8 pa3) {
;     ...
;     o0 = __builtin_amdgcn_mfma_f32_32x32x16_bf16(pa0, PK(a0, b0), o0, 0, 0, 0);
;     o0 = __builtin_amdgcn_mfma_f32_32x32x16_bf16(pa1, PK(a1, b1), o0, 0, 0, 0);
;     o0 = __builtin_amdgcn_mfma_f32_32x32x16_bf16(pa2, PK(a2, b2), o0, 0, 0, 0);
;     o0 = __builtin_amdgcn_mfma_f32_32x32x16_bf16(pa3, PK(a3, b3), o0, 0, 0, 0);
;     asm volatile("s_waitcnt lgkmcnt(0)" ::: "memory"); SBAR();
;     o1 = __builtin_amdgcn_mfma_f32_32x32x16_bf16(pa0, PK(c0, d0), o1, 0, 0, 0);
;     o1 = __builtin_amdgcn_mfma_f32_32x32x16_bf16(pa1, PK(c1, d1), o1, 0, 0, 0);
;     o1 = __builtin_amdgcn_mfma_f32_32x32x16_bf16(pa2, PK(c2, d2), o1, 0, 0, 0);
;     o1 = __builtin_amdgcn_mfma_f32_32x32x16_bf16(pa3, PK(c3, d3), o1, 0, 0, 0);
;     ...
; }
; template <bool FIRST> DEVI bool partialSM(f32x16& p0, f32x16& p1, float& m_reg, float& alpha) {
;     float pmax = p0[0];
; #pragma unroll
;     for (int r = 1; r < 16; ++r) pmax = fmaxf(pmax, p0[r]);
; #pragma unroll
;     for (int r = 0; r < 16; ++r) pmax = fmaxf(pmax, p1[r]);
;     { auto rr = __builtin_amdgcn_permlane32_swap(__float_as_uint(pmax), __float_as_uint(pmax), false, false);
;       pmax = fmaxf(__uint_as_float(rr[0]), __uint_as_float(rr[1])); }
	s_waitcnt lgkmcnt(14)
	v_mfma_f32_32x32x16_bf16 v[18:33], v[50:53], v[154:157], v[18:33]
	v_permlane32_swap_b32_e32 v126, v127
	s_waitcnt lgkmcnt(6)
	v_mfma_f32_32x32x16_bf16 v[2:17], v[50:53], v[210:213], v[2:17]
	s_nop 1
	v_max_f32_e32 v249, v99, v99
	v_max_f32_e32 v250, v98, v98
	v_max_f32_e32 v249, v250, v249
	v_max3_f32 v249, v249, v100, v101
	v_max3_f32 v249, v249, v102, v103
	v_max3_f32 v251, v249, v104, v105
	v_max3_f32 v251, v251, v106, v107
	v_exp_f32_e32 v50, v98
	v_exp_f32_e32 v51, v99
	v_exp_f32_e32 v52, v100
	v_exp_f32_e32 v53, v101
	v_mfma_f32_32x32x16_bf16 v[18:33], v[54:57], v[158:161], v[18:33]
	s_waitcnt lgkmcnt(4)
	v_mfma_f32_32x32x16_bf16 v[2:17], v[54:57], v[214:217], v[2:17]
	v_max3_f32 v251, v251, v108, v109
	v_max3_f32 v251, v251, v110, v111
	v_max3_f32 v251, v251, v112, v113
	v_max3_f32 v251, v251, v66, v67
	v_max3_f32 v251, v251, v68, v69
	v_max3_f32 v251, v251, v70, v71
	v_max3_f32 v251, v251, v72, v73
	v_exp_f32_e32 v54, v102
	v_exp_f32_e32 v55, v103
	v_exp_f32_e32 v56, v104
	v_exp_f32_e32 v57, v105
	v_mfma_f32_32x32x16_bf16 v[18:33], v[58:61], v[162:165], v[18:33]
	s_waitcnt lgkmcnt(2)
	v_mfma_f32_32x32x16_bf16 v[2:17], v[58:61], v[218:221], v[2:17]
	v_max3_f32 v251, v251, v74, v75
	v_max3_f32 v251, v251, v76, v77
	v_max3_f32 v251, v251, v78, v79
	v_max3_f32 v251, v251, v80, v81
	v_mov_b32_e32 v252, v251


; #define SBAR() __builtin_amdgcn_sched_barrier(0)
; DEVI void pv_both(f32x16& o0, f32x16& o1, int vb, bf16x8 pa0, bf16x8 pa1, bf16x8 pa2, bf16x8 pa3) {
;     ...
;     asm volatile("s_waitcnt lgkmcnt(0)" ::: "memory"); SBAR();
;     o1 = __builtin_amdgcn_mfma_f32_32x32x16_bf16(pa0, PK(c0, d0), o1, 0, 0, 0);
;     o1 = __builtin_amdgcn_mfma_f32_32x32x16_bf16(pa1, PK(c1, d1), o1, 0, 0, 0);
;     o1 = __builtin_amdgcn_mfma_f32_32x32x16_bf16(pa2, PK(c2, d2), o1, 0, 0, 0);
;     o1 = __builtin_amdgcn_mfma_f32_32x32x16_bf16(pa3, PK(c3, d3), o1, 0, 0, 0);
;     ...
; }
; template <bool FIRST> DEVI bool partialSM(f32x16& p0, f32x16& p1, float& m_reg, float& alpha) {
;     float pmax = p0[0];
; #pragma unroll
;     for (int r = 1; r < 16; ++r) pmax = fmaxf(pmax, p0[r]);
; #pragma unroll
;     for (int r = 0; r < 16; ++r) pmax = fmaxf(pmax, p1[r]);
;     { auto rr = __builtin_amdgcn_permlane32_swap(__float_as_uint(pmax), __float_as_uint(pmax), false, false);
;       pmax = fmaxf(__uint_as_float(rr[0]), __uint_as_float(rr[1])); }
;     if (FIRST) { m_reg = pmax; alpha = 1.f;
; #pragma unroll
;         for (int r = 0; r < 16; ++r) { p0[r] = __builtin_amdgcn_exp2f(p0[r] - pmax); p1[r] = p1[r] - pmax; }
;         return false;
;     } else if (__builtin_expect(__all(pmax <= ATT_THR), 1)) { alpha = 1.f;
; #pragma unroll
;         for (int r = 0; r < 16; ++r) p0[r] = __builtin_amdgcn_exp2f(p0[r]);
;         return false;
	v_exp_f32_e32 v58, v106
	v_exp_f32_e32 v59, v107
	v_permlane32_swap_b32_e32 v251, v252
	v_exp_f32_e32 v60, v108
	v_exp_f32_e32 v61, v109
	v_mfma_f32_32x32x16_bf16 v[18:33], v[62:65], v[166:169], v[18:33]
	s_waitcnt lgkmcnt(0)
	v_mfma_f32_32x32x16_bf16 v[2:17], v[62:65], v[222:225], v[2:17]
	v_exp_f32_e32 v62, v110
	v_exp_f32_e32 v63, v111
	v_exp_f32_e32 v64, v112
	v_exp_f32_e32 v65, v113
	v_max_f32_e32 v252, v252, v252
	v_max_f32_e32 v251, v251, v251
	v_max_f32_e32 v174, v251, v252
	v_cmp_ge_f32_e32 vcc, s79, v174
	s_cmp_lg_u64 vcc, exec
	s_cselect_b64 s[6:7], -1, 0
	s_cbranch_scc1 .LBB0_711
	v_mov_b32_e32 v202, 1.0
	v_mov_b32_e32 v203, v209
	s_branch .LBB0_716

; DEVI void cv_finish(char* img  , int lane, const CvRegs& R) {
;     ...
;     const int n = lane >> 1, half = lane & 1; u32x4 w0, w1;
; #pragma unroll
;     for (int j = 0; j < 4; ++j) { w0[j] = *(const unsigned*)(img + n * 68 + half * 32 + j * 4); w1[j] = *(const unsigned*)(img + n * 68 + half * 32 + 16 + j * 4); }
;     const int row = R.c.perm ? R.c.r0 + 128 * ((n >> 3) & 1) + 16 * ((n >> 2) & 1) + 4 * (n >> 4) + (n & 3) : R.c.r0 + 128 * ((n >> 2) & 1) + 4 * (n >> 3) + (n & 3);
;     bf16_t* d = R.c.dst + (size_t)row * R.c.K + R.c.k0 + half * 16;
.Lmy_cvj_a:
	ds_read2_b32 v[66:67], v68 offset1:1
	ds_read2_b32 v[70:71], v68 offset0:4 offset1:5
	ds_read2_b32 v[72:73], v68 offset0:6 offset1:7
	ds_read2_b32 v[68:69], v68 offset0:2 offset1:3


; #define VM0() asm volatile("s_waitcnt vmcnt(0)" ::: "memory")
; DEVI void cv_finish(char* img  , int lane, const CvRegs& R) {
;     ...
;     bf16_t* d = R.c.dst + (size_t)row * R.c.K + R.c.k0 + half * 16;
;     __builtin_nontemporal_store(w0, (u32x4*)d); __builtin_nontemporal_store(w1, (u32x4*)(d + 8));
;     asm volatile("" ::: "memory"); __builtin_amdgcn_wave_barrier();
; DEVI void attn_unit8(const Params& p, char* smem, int unit, int l, int& cvs  , CvRun& crun) {
;     ...
;         if (cvr.live) asm volatile("s_waitcnt vmcnt(2)" ::: "memory"); else VM0();
	s_waitcnt lgkmcnt(0)
	global_store_dwordx4 v246, v[66:69], s[40:41] nt
	global_store_dwordx4 v246, v[70:73], s[40:41] offset:16 nt
	s_waitcnt vmcnt(2)
	s_cbranch_execz .LBB0_701
	s_branch .LBB0_702

; DEVI f32x4 ld_nt(const float* p) { return __builtin_nontemporal_load((const f32x4*)p); }
; DEVI void cv_next(const Params& p, int l, int s, int lane, int stride, CvRun& run) {
;     ...
;     run.c = cv_slice(p, l, s, lane); run.left = 0;
;     if ((stride & 511) == 0) {
;         if (s < NS_W13) { const int e = s >> 9, es = stride >> 9; if (e < NE) { run.left = (NE - 1 - e) / es; run.sstep = (long)es * 1024 * 256; run.dstep = (long)es * 512 * 1024; } }
;         else { const int e = (s - NS_W13) >> 8, es = stride >> 8; if (e < NE) { run.left = (NE - 1 - e) / es; run.sstep = (long)es * 256 * 1024; run.dstep = (long)es * 1024 * 256; } } }
; }
; DEVI void cv_issue(const Params& p, int l, int s, int lane, CvRegs& R, CvRun& run) {
;     R.live = s < NS_SLICES ? 1 : 0;
;     if (R.live) { cv_next(p, l, s, lane, (int)gridDim.x * 8, run); R.c = run.c; const int kq = lane >> 3;
;         const float* sp = R.c.src + (size_t)(R.c.k0 + 2 * kq) * R.c.ld;
;         R.a0 = ld_nt(sp); R.b0 = ld_nt(sp + R.c.ld); R.a1 = ld_nt(sp + (size_t)16 * R.c.ld); R.b1 = ld_nt(sp + (size_t)17 * R.c.ld); }
.LBB0_718:
	v_mov_b32_e32 v172, s40
	v_mov_b32_e32 v173, s41
	s_mov_b64 s[44:45], 0x4000
	v_lshlrev_b32_e32 v250, 2, v114
	v_mov_b32_e32 v251, 0
	v_lshl_add_u64 v[170:171], s[68:69], 0, v[250:251]
	s_cmp_lt_i32 s54, 0x30300
	s_cselect_b64 s[12:13], -1, 0
	s_cmp_gt_i32 s54, 0x302ff
	s_cbranch_scc1 .LBB0_748
	s_cmp_gt_i32 s56, 0
	s_mov_b64 s[14:15], -1
	s_cbranch_scc1 .LBB0_745
	s_cmp_gt_i32 s54, 0x201ff
	s_cselect_b64 s[14:15], -1, 0
	s_cmp_lt_i32 s54, 0x20200
	s_mov_b64 s[6:7], -1
	s_cbranch_scc1 .LBB0_722
	s_add_i32 s2, s54, 0xfffdfe00
	s_lshr_b32 s8, s2, 8
	s_and_b32 s10, s54, 0xe0
	s_cmp_lt_u32 s2, 0x10000
	s_cselect_b64 s[6:7], -1, 0
	s_lshl_b32 s2, s2, 10
	s_and_b32 s2, s2, 0x3fc0000
	s_and_b64 s[6:7], s[6:7], exec
	s_cselect_b32 s6, 0xc0, s78
	s_cselect_b32 s2, s2, 0
	s_add_u32 s6, s24, s6
	s_addc_u32 s7, s25, 0
	s_load_dwordx2 s[6:7], s[6:7], 0x0
	s_lshl_b32 s2, s2, 2
	s_load_dwordx2 s[18:19], s[24:25], 0x158
	s_waitcnt lgkmcnt(0)
	s_add_u32 s2, s6, s2
	s_addc_u32 s6, s7, 0
	s_lshl_b32 s7, s54, 7
	s_lshl_b32 s11, s54, 5
	s_and_b32 s7, s7, 0xf80
	s_add_u32 s16, s2, s7
	s_addc_u32 s17, s6, 0
	s_lshl_b64 s[6:7], s[8:9], 19
	s_add_u32 s18, s18, s6
	s_addc_u32 s19, s19, s7
	s_lshl_b32 s6, s54, 4
	s_and_b32 s2, s11, 0x300
	s_and_b32 s6, s6, 0x60
	s_or_b32 s2, s2, s6
	s_lshl_b32 s6, s54, 3
	s_and_b32 s6, s6, 8
	s_or_b32 s8, s2, s6
	s_mov_b64 s[6:7], 0

; DEVI void cv_next(const Params& p, int l, int s, int lane, int stride, CvRun& run) {
;     ...
;     run.c = cv_slice(p, l, s, lane); run.left = 0;
;     if ((stride & 511) == 0) {
;         if (s < NS_W13) { const int e = s >> 9, es = stride >> 9; if (e < NE) { run.left = (NE - 1 - e) / es; run.sstep = (long)es * 1024 * 256; run.dstep = (long)es * 512 * 1024; } }
;         else { const int e = (s - NS_W13) >> 8, es = stride >> 8; if (e < NE) { run.left = (NE - 1 - e) / es; run.sstep = (long)es * 256 * 1024; run.dstep = (long)es * 1024 * 256; } } }
.LBB0_744:
	v_lshlrev_b32_e32 v174, 2, v114
	v_lshl_add_u64 v[82:83], s[16:17], 0, v[174:175]
	s_mov_b64 s[68:69], s[16:17]
	s_mov_b64 s[14:15], 0
	v_mov_b64_e32 v[182:183], s[18:19]
	s_mov_b64 s[40:41], s[18:19]
.LBB0_745:
	s_and_b64 vcc, exec, s[14:15]
	s_cbranch_vccz .LBB0_747
	s_lshl_b64 s[6:7], s[26:27], 1
	v_lshl_add_u64 v[82:83], s[28:29], 2, v[170:171]
	s_lshl_b64 s[14:15], s[28:29], 2
	s_add_u32 s68, s68, s14
	s_addc_u32 s69, s69, s15
	v_lshl_add_u64 v[182:183], v[172:173], 0, s[6:7]
	s_add_u32 s40, s40, s6
	s_addc_u32 s41, s41, s7
	s_add_i32 s2, s56, -1
	s_mov_b32 s8, s60
	s_mov_b32 s94, s59
	s_mov_b32 s10, s58
	s_mov_b32 s6, s57
	s_mov_b32 s95, s55
	s_mov_b64 s[22:23], s[28:29]
	s_mov_b64 s[20:21], s[26:27]

; DEVI int tidx() { int t = threadIdx.x; asm volatile("" : "+v"(t)); __builtin_assume(t >= 0 && t < 512); return t; }
; DEVI unsigned cvt_pk_bf16(float lo, float hi) { unsigned r; asm volatile("v_cvt_pk_bf16_f32 %0, %1, %2" : "=v"(r) : "v"(lo), "v"(hi)); return r; }
; DEVI float bf2f(bf16_t h) { return __uint_as_float(((unsigned)h) << 16); }
; DEVI void attn_unit8(const Params& p, char* smem, int unit, int l, int& cvs  , CvRun& crun) {
;     const int tid = tidx(), wid = __builtin_amdgcn_readfirstlane(tid >> 6), lane = tid & 63, r32 = lane & 31, hi = lane >> 5;
;     const int x8 = unit & 7, v8 = unit >> 3, bh = x8 + 8 * (v8 >> 4), qt = v8 & 15, b = bh >> 3, hh = bh & 7;
;     char* K_lds = smem; char* V_lds = smem + 73728;
;     float* wsx = (float*)(smem + 122880) + wid * 64; float* li_l = wsx; float* al_l = wsx + 32;
;     const bf16_t* Kg = p.kfull + (size_t)bh * S_ * 96; const bf16_t* Vg = p.vfull + (size_t)bh * S_ * 64;
;     const size_t qtok = (size_t)b * S_ + qt * 256 + wid * 32 + r32;
;     bf16x8 qr[6];
;     { const bf16_t* qp = p.qbuf + qtok * 768 + hh * 96 + hi * 8;
; #pragma unroll
;       for (int d0 = 0; d0 < 6; ++d0) qr[d0] = *(const bf16x8*)(qp + d0 * 16);
;       const f32x4 c0 = *(const f32x4*)(p.cs + qtok * 16 + hi * 8), c1 = *(const f32x4*)(p.cs + qtok * 16 + hi * 8 + 4);
;       const f32x4 s0 = *(const f32x4*)(p.sn + qtok * 16 + hi * 8), s1 = *(const f32x4*)(p.sn + qtok * 16 + hi * 8 + 4);
;       float o1[8], o2[8];
; #pragma unroll
;       for (int j = 0; j < 8; ++j) { const float x1 = bf2f((bf16_t)qr[4][j]), x2 = bf2f((bf16_t)qr[5][j]); const float cc = j < 4 ? c0[j] : c1[j - 4], ss = j < 4 ? s0[j] : s1[j - 4];
;           o1[j] = x1 * cc - x2 * ss; o2[j] = x2 * cc + x1 * ss; }
;       u32x4 w1, w2;
; #pragma unroll
;       for (int j = 0; j < 4; ++j) { w1[j] = cvt_pk_bf16(o1[2 * j], o1[2 * j + 1]); w2[j] = cvt_pk_bf16(o2[2 * j], o2[2 * j + 1]); }
;       qr[4] = *(bf16x8*)&w1; qr[5] = *(bf16x8*)&w2; }
.LBB0_2229:
	v_mov_b32_e32 v86, v0
	s_ashr_i32 s5, s87, 4
	v_readfirstlane_b32 s4, v86
	s_lshr_b32 s53, s4, 6
	s_and_b32 s52, s5, -8
	s_and_b32 s8, s4, 0x3fffffc0
	s_load_dwordx4 s[4:7], s[24:25], 0x1a0
	s_load_dwordx4 s[12:15], s[24:25], 0x110
	s_and_b32 s92, s87, 7
	s_ashr_i32 s16, s87, 7
	s_lshl_b32 s8, s8, 2
	s_or_b32 s10, s52, s92
	s_add_i32 s93, s8, 0
	s_ashr_i32 s17, s16, 31
	s_lshl_b32 s8, s87, 5
	s_ashr_i32 s11, s10, 31
	s_lshl_b64 s[16:17], s[16:17], 12
	s_and_b32 s8, s8, 0xf00
	s_and_b32 s2, s62, 7
	s_add_i32 s93, s93, 0x1e000
	s_waitcnt lgkmcnt(0)
	v_mov_b32_e32 v2, s4
	v_mov_b32_e32 v3, s5
	s_lshl_b64 s[4:5], s[10:11], 19
	s_or_b32 s8, s16, s8
	s_lshl_b32 s11, s53, 5
	v_and_b32_e32 v176, 31, v86
	s_add_u32 s48, s8, s11
	v_or_b32_e32 v10, s48, v176
	s_addc_u32 s49, s17, 0
	v_mad_u64_u32 v[2:3], s[16:17], v10, s74, v[2:3]
	v_bfe_u32 v187, v86, 5, 1
	v_mad_i32_i24 v3, s49, v181, v3
	s_mul_i32 s8, s92, 0xc0
	v_mov_b32_e32 v11, s49
	v_lshl_add_u64 v[2:3], v[2:3], 0, s[8:9]
	v_lshlrev_b32_e32 v178, 4, v187
	v_mov_b32_e32 v179, v175
	v_lshl_add_u64 v[26:27], v[2:3], 0, v[178:179]
	v_lshlrev_b64 v[10:11], 6, v[10:11]
	global_load_dwordx4 v[2:5], v[26:27], off offset:128
	global_load_dwordx4 v[6:9], v[26:27], off offset:160
	v_lshl_add_u64 v[12:13], s[12:13], 0, v[10:11]
	v_and_b32_e32 v174, 32, v86
	v_lshl_add_u64 v[10:11], s[14:15], 0, v[10:11]
	v_lshl_add_u64 v[22:23], v[12:13], 0, v[174:175]
	v_lshl_add_u64 v[18:19], v[10:11], 0, v[174:175]
	global_load_dwordx4 v[10:13], v[18:19], off
	global_load_dwordx4 v[14:17], v[22:23], off
	s_nop 0
	global_load_dwordx4 v[18:21], v[18:19], off offset:16
	s_nop 0
	global_load_dwordx4 v[22:25], v[22:23], off offset:16
	s_load_dwordx2 s[50:51], s[24:25], 0x1b0
	global_load_dwordx4 v[150:153], v[26:27], off
	global_load_dwordx4 v[138:141], v[26:27], off offset:32
	global_load_dwordx4 v[134:137], v[26:27], off offset:64
	global_load_dwordx4 v[130:133], v[26:27], off offset:96
	s_mul_hi_i32 s8, s10, 0xc0000
	s_mul_i32 s10, s10, 0xc0000
	s_add_u32 s10, s6, s10
	s_addc_u32 s11, s7, s8
	s_lshl_b32 s61, s53, 10
	s_add_i32 s96, s61, 0
	s_waitcnt lgkmcnt(0)
	s_add_u32 s4, s50, s4
	s_mov_b32 m0, s96
	v_lshlrev_b32_e32 v88, 6, v187
	s_addc_u32 s5, s51, s5
	s_add_i32 s97, s76, s61
	v_lshlrev_b32_e32 v90, 2, v86
	v_and_b32_e32 v91, 63, v86
	v_lshlrev_b32_e32 v93, 4, v91
	v_lshlrev_b32_e32 v92, 3, v91
	v_lshlrev_b32_e32 v94, 1, v91
	s_mov_b32 s8, s9
	s_mov_b32 s12, s9
	s_mov_b32 s13, s9
	s_mov_b32 s14, s9
	s_mov_b32 s15, s9
	s_mov_b32 s16, s9
	s_mov_b32 s17, s9
	s_mov_b32 s18, s9
	s_mov_b32 s19, s9
	s_mov_b32 s20, s9
	s_mov_b32 s21, s9
	s_mov_b32 s22, s9
	s_mov_b32 s23, s9
	s_mulk_i32 s53, 0x900
	v_mov_b32_e32 v83, v175
	v_mov_b32_e32 v85, v175
	v_and_b32_e32 v114, 28, v90
	v_lshl_add_u32 v188, v176, 2, s93
	v_mul_u32_u24_e32 v202, 0x44, v114
	v_bfe_u32 v196, v91, 1, 2
	v_mov_b32_e32 v208, 1.0
	s_mov_b32 s71, s9
	v_mov_b32_e32 v189, v175
	s_waitcnt vmcnt(9)
	v_lshlrev_b32_e32 v27, 16, v2
	s_waitcnt vmcnt(8)
	v_lshlrev_b32_e32 v26, 16, v6
	v_and_b32_e32 v33, 0xffff0000, v2
	v_lshlrev_b32_e32 v35, 16, v3
	s_waitcnt vmcnt(7)
	v_mov_b32_e32 v28, v10
	s_waitcnt vmcnt(6)
	v_mov_b32_e32 v29, v14
	v_mov_b32_e32 v36, v12
	v_mov_b32_e32 v37, v16
	v_mov_b32_e32 v38, v16
	v_mov_b32_e32 v39, v12
	v_and_b32_e32 v3, 0xffff0000, v3
	v_and_b32_e32 v2, 0xffff0000, v7
	v_mov_b32_e32 v16, v13
	v_mov_b32_e32 v12, v17
	v_and_b32_e32 v32, 0xffff0000, v6
	v_lshlrev_b32_e32 v34, 16, v7
	v_pk_mul_f32 v[6:7], v[28:29], v[26:27]
	v_pk_mul_f32 v[16:17], v[16:17], v[2:3]
	v_pk_mul_f32 v[2:3], v[12:13], v[2:3]
	v_mov_b32_e32 v30, v14
	v_mov_b32_e32 v31, v10
	v_sub_f32_e32 v12, v7, v6
	v_sub_f32_e32 v16, v17, v16
	v_add_f32_e32 v17, v2, v3
	v_lshlrev_b32_e32 v3, 16, v4
	v_lshlrev_b32_e32 v2, 16, v8
	s_waitcnt vmcnt(5)
	v_mov_b32_e32 v6, v18
	s_waitcnt vmcnt(4)
	v_mov_b32_e32 v7, v22
	v_pk_mul_f32 v[26:27], v[30:31], v[26:27]
	v_pk_mul_f32 v[6:7], v[6:7], v[2:3]
	v_add_f32_e32 v13, v26, v27
	v_sub_f32_e32 v26, v7, v6
	v_mov_b32_e32 v6, v22
	v_mov_b32_e32 v7, v18
	v_pk_mul_f32 v[2:3], v[6:7], v[2:3]
	v_mov_b32_e32 v22, v19
	v_add_f32_e32 v27, v2, v3
	v_and_b32_e32 v3, 0xffff0000, v4
	v_and_b32_e32 v2, 0xffff0000, v8
	v_mov_b32_e32 v18, v23
	v_pk_mul_f32 v[6:7], v[22:23], v[2:3]
	v_pk_mul_f32 v[2:3], v[18:19], v[2:3]
	v_sub_f32_e32 v8, v7, v6
	v_add_f32_e32 v18, v2, v3
	v_lshlrev_b32_e32 v3, 16, v5
	v_lshlrev_b32_e32 v2, 16, v9
	v_mov_b32_e32 v6, v20
	v_mov_b32_e32 v7, v24
	v_pk_mul_f32 v[6:7], v[6:7], v[2:3]
	v_mov_b32_e32 v14, v11
	v_sub_f32_e32 v19, v7, v6
	v_mov_b32_e32 v6, v24
	v_mov_b32_e32 v7, v20
	v_pk_mul_f32 v[2:3], v[6:7], v[2:3]
	v_mov_b32_e32 v24, v21
	v_add_f32_e32 v6, v2, v3
	v_and_b32_e32 v3, 0xffff0000, v5
	v_and_b32_e32 v2, 0xffff0000, v9
	v_mov_b32_e32 v20, v25
	v_mov_b32_e32 v10, v15
	v_pk_mul_f32 v[4:5], v[24:25], v[2:3]
	v_pk_mul_f32 v[2:3], v[20:21], v[2:3]
	v_pk_mul_f32 v[14:15], v[14:15], v[32:33]
	v_pk_mul_f32 v[10:11], v[10:11], v[32:33]
	v_pk_mul_f32 v[28:29], v[36:37], v[34:35]
	v_pk_mul_f32 v[30:31], v[38:39], v[34:35]
	v_add_f32_e32 v2, v2, v3
	v_sub_f32_e32 v14, v15, v14
	v_add_f32_e32 v10, v10, v11
	v_sub_f32_e32 v11, v29, v28
	v_add_f32_e32 v15, v30, v31
	v_sub_f32_e32 v4, v5, v4
	v_cvt_pk_bf16_f32 v146, v12, v14
	v_cvt_pk_bf16_f32 v142, v13, v10
	v_cvt_pk_bf16_f32 v147, v11, v16
	v_cvt_pk_bf16_f32 v143, v15, v17
	v_cvt_pk_bf16_f32 v148, v26, v8
	v_cvt_pk_bf16_f32 v144, v27, v18
	v_cvt_pk_bf16_f32 v149, v19, v4
	v_cvt_pk_bf16_f32 v145, v6, v2
	v_mul_u32_u24_e32 v2, 0xaaab, v86
	v_lshrrev_b32_e32 v3, 19, v2
	v_mul_lo_u16_e32 v4, 12, v3
	v_sub_u16_e32 v4, v86, v4
	v_lshrrev_b32_e32 v2, 21, v2
; #define LAS __attribute__((address_space(3)))
; DEVI int v_rd_base(int lane) { return ((lane & 3) << 3) | (((lane >> 2) & 3) << 6) | (((lane >> 4) & 1) << 5) | (((lane >> 5) & 1) << 8); }
; #define VM0() asm volatile("s_waitcnt vmcnt(0)" ::: "memory")
; DEVI void attn_unit8(const Params& p, char* smem, int unit, int l, int& cvs  , CvRun& crun) {
;     ...
;     int ksrc[3];
; #pragma unroll
;     for (int i = 0; i < 3; ++i) { const int pc = tid + 512 * i, row = pc / 12, ch = (pc % 12) ^ ((row >> 2) & 3); ksrc[i] = row * 192 + ch * 16; }
;     const int vsrc = wid * 1024 + ((lane >> 2) & 7) * 128 + (lane >> 5) * 64 + (lane & 3) * 16;
;     LAS char* const Kl = (LAS char*)K_lds + wid * 1024; LAS char* const Vl = (LAS char*)V_lds + wid * 1024;
;     ...
;     const int vb0 = (int)(uintptr_t)(LAS char*)V_lds + v_rd_base(lane);
;     float m_reg = 0.f, l_reg = 0.f; f32x16 o[2];
; #pragma unroll
;     for (int d = 0; d < 2; ++d)
; #pragma unroll
;         for (int r = 0; r < 16; ++r) o[d][r] = 0.f;
;     f32x16 pA0, pA1, pB0, pB1; float alA, alB; bf16x8 pa0, pa1, pa2, pa3;
;     constexpr int NTILE = S_ / 128;
;     B_DMA(0, 0); B_DMA(1, 1); VM0(); __syncthreads();
	v_bitop3_b32 v2, v2, v4, 3 bitop3:0x6c
	v_mul_u32_u24_e32 v3, 0xc0, v3
	v_lshl_add_u32 v174, v2, 4, v3
	v_or_b32_e32 v2, 0x200, v86
	v_mul_u32_u24_sdwa v3, v2, s75 dst_sel:DWORD dst_unused:UNUSED_PAD src0_sel:WORD_0 src1_sel:DWORD
	v_lshrrev_b32_e32 v4, 19, v3
	v_mul_lo_u16_e32 v5, 12, v4
	v_sub_u16_e32 v2, v2, v5
	v_lshrrev_b32_e32 v3, 21, v3
	v_bitop3_b32 v2, v3, v2, 3 bitop3:0x6c
	v_mul_u32_u24_e32 v3, 0xc0, v4
	v_lshl_add_u32 v82, v2, 4, v3
	v_or_b32_e32 v2, 0x400, v86
	v_mul_u32_u24_sdwa v3, v2, s75 dst_sel:DWORD dst_unused:UNUSED_PAD src0_sel:WORD_0 src1_sel:DWORD
	v_lshrrev_b32_e32 v4, 19, v3
	v_mul_lo_u16_e32 v5, 12, v4
	v_sub_u16_e32 v2, v2, v5
	v_lshrrev_b32_e32 v3, 21, v3
	v_bitop3_b32 v2, v3, v2, 3 bitop3:0x6c
	v_mul_u32_u24_e32 v3, 0xc0, v4
	v_lshl_add_u32 v84, v2, 4, v3
	v_lshlrev_b32_e32 v2, 5, v86
	v_and_b32_e32 v87, 0x380, v2
	v_lshlrev_b32_e32 v3, 4, v86
	global_load_lds_dwordx4 v174, s[10:11]
	s_add_i32 m0, s96, 0x2000
	v_or_b32_e32 v2, v88, v87
	v_and_b32_e32 v89, 48, v3
	global_load_lds_dwordx4 v82, s[10:11]
	s_add_i32 m0, s96, 0x4000
	v_or3_b32 v2, v2, v89, s61
	global_load_lds_dwordx4 v84, s[10:11]
	v_mov_b32_e32 v3, v175
	s_mov_b32 m0, s97
	v_lshl_add_u64 v[4:5], s[4:5], 0, v[2:3]
	global_load_lds_dwordx4 v2, s[4:5]
	s_add_i32 m0, s97, 0x2000
	s_mov_b64 s[72:73], 0x2000
	v_lshl_add_u64 v[2:3], v[4:5], 0, s[72:73]
	s_add_u32 s4, s10, 0x6000
	global_load_lds_dwordx4 v[2:3], off
	s_addc_u32 s5, s11, 0
	s_add_i32 m0, s96, 0x6000
	v_lshl_add_u64 v[2:3], v[4:5], 0, s[44:45]
	global_load_lds_dwordx4 v174, s[4:5]
	s_add_i32 m0, s96, 0x8000
	v_mul_u32_u24_e32 v10, 0xc0, v176
	global_load_lds_dwordx4 v82, s[4:5]
	s_add_i32 m0, s96, 0xa000
	v_and_b32_e32 v11, 48, v90
	global_load_lds_dwordx4 v84, s[4:5]
	s_add_i32 m0, s97, 0x4000
	v_bitop3_b32 v129, v178, v10, v11 bitop3:0xde
	global_load_lds_dwordx4 v[2:3], off
	v_lshl_add_u64 v[2:3], v[4:5], 0, s[42:43]
	s_add_i32 m0, s97, 0x6000
	v_add_u32_e32 v190, 0, v129
	global_load_lds_dwordx4 v[2:3], off
	s_waitcnt vmcnt(0)
	s_waitcnt vmcnt(0) lgkmcnt(0)
	s_barrier
; template <bool FIRST> DEVI bool partialSM(f32x16& p0, f32x16& p1, float& m_reg, float& alpha) {
;     float pmax = p0[0];
; #pragma unroll
;     for (int r = 1; r < 16; ++r) pmax = fmaxf(pmax, p0[r]);
; #pragma unroll
;     for (int r = 0; r < 16; ++r) pmax = fmaxf(pmax, p1[r]);
;     { auto rr = __builtin_amdgcn_permlane32_swap(__float_as_uint(pmax), __float_as_uint(pmax), false, false);
;       pmax = fmaxf(__uint_as_float(rr[0]), __uint_as_float(rr[1])); }
;     if (FIRST) { m_reg = pmax; alpha = 1.f;
; #pragma unroll
;         for (int r = 0; r < 16; ++r) { p0[r] = __builtin_amdgcn_exp2f(p0[r] - pmax); p1[r] = p1[r] - pmax; }
;         return false;
; DEVI void qkt(f32x16& p0, f32x16& p1, const char* Kb, const bf16x8 (&qr)[6], int r32, int hi, const f32x16& cinit) {
; #pragma unroll
;     for (int d0 = 0; d0 < 6; ++d0) { const int cb = (d0 * 16 + hi * 8) * 2;
;         const bf16x8 k0 = *(const bf16x8*)(Kb + KSWZ(r32, cb)), k1 = *(const bf16x8*)(Kb + KSWZ(32 + r32, cb));
;         p0 = __builtin_amdgcn_mfma_f32_32x32x16_bf16(k0, qr[d0], d0 == 0 ? cinit : p0, 0, 0, 0);
;         p1 = __builtin_amdgcn_mfma_f32_32x32x16_bf16(k1, qr[d0], d0 == 0 ? cinit : p1, 0, 0, 0); }
; }
	ds_read_b128 v[2:5], v190
	ds_read_b128 v[6:9], v190 offset:6144
	s_waitcnt lgkmcnt(1)
	v_mfma_f32_32x32x16_bf16 v[34:49], v[2:5], v[150:153], 0
	v_or_b32_e32 v2, 32, v178
	v_bitop3_b32 v184, v2, v10, v11 bitop3:0xde
	v_add_u32_e32 v191, 0, v184
	s_mov_b32 s10, s9
	s_mov_b32 s11, s9
	s_lshl_b32 s84, s54, 5
	s_lshl_b32 s85, s54, 4
	s_waitcnt lgkmcnt(0)
	v_mfma_f32_32x32x16_bf16 v[18:33], v[6:9], v[150:153], 0
	ds_read_b128 v[2:5], v191
	ds_read_b128 v[6:9], v191 offset:6144
	s_lshl_b32 s88, s54, 3
	s_lshl_b32 s70, s54, 1
	v_cmp_gt_u32_e64 s[4:5], 32, v91
	s_waitcnt lgkmcnt(1)
	v_mfma_f32_32x32x16_bf16 v[34:49], v[2:5], v[138:141], v[34:49]
	v_or_b32_e32 v2, 64, v178
	v_xad_u32 v185, v2, v11, v10
	v_add_u32_e32 v192, 0, v185
	s_waitcnt lgkmcnt(0)
	v_mfma_f32_32x32x16_bf16 v[18:33], v[6:9], v[138:141], v[18:33]
	ds_read_b128 v[2:5], v192
	ds_read_b128 v[6:9], v192 offset:6144
	s_waitcnt lgkmcnt(1)
	v_mfma_f32_32x32x16_bf16 v[34:49], v[2:5], v[134:137], v[34:49]
	v_or_b32_e32 v2, 0x60, v178
	v_xad_u32 v205, v2, v11, v10
	v_add_u32_e32 v193, 0, v205
	ds_read_b128 v[2:5], v193
	s_waitcnt lgkmcnt(1)
	v_mfma_f32_32x32x16_bf16 v[18:33], v[6:9], v[134:137], v[18:33]
	ds_read_b128 v[6:9], v193 offset:6144
	s_waitcnt lgkmcnt(1)
	v_mfma_f32_32x32x16_bf16 v[34:49], v[2:5], v[130:133], v[34:49]
	v_and_b32_e32 v2, 0xc0, v93
	v_and_or_b32 v12, v92, 24, v2
	v_or_b32_e32 v2, 0x80, v178
	v_xad_u32 v206, v2, v11, v10
	v_add_u32_e32 v194, 0, v206
	ds_read_b128 v[2:5], v194
	s_waitcnt lgkmcnt(1)
	v_mfma_f32_32x32x16_bf16 v[18:33], v[6:9], v[130:133], v[18:33]
	v_and_b32_e32 v6, 32, v94
	v_and_b32_e32 v7, 0x100, v92
	v_or3_b32 v179, v12, v6, v7
	ds_read_b128 v[6:9], v194 offset:6144
	v_add_u32_e32 v115, s76, v179
	s_waitcnt lgkmcnt(1)
	v_mfma_f32_32x32x16_bf16 v[34:49], v[2:5], v[146:149], v[34:49]
	v_or_b32_e32 v2, 0xa0, v178
	v_xad_u32 v207, v2, v11, v10
	v_add_u32_e32 v195, 0, v207
	ds_read_b128 v[2:5], v195
	ds_read_b128 v[50:53], v195 offset:6144
	s_waitcnt lgkmcnt(2)
	v_mfma_f32_32x32x16_bf16 v[18:33], v[6:9], v[146:149], v[18:33]
	s_waitcnt lgkmcnt(1)
	v_mfma_f32_32x32x16_bf16 v[34:49], v[2:5], v[142:145], v[34:49]
	v_mov_b64_e32 v[2:3], s[8:9]
	v_mov_b64_e32 v[4:5], s[10:11]
	v_mov_b64_e32 v[6:7], s[12:13]
	v_mov_b64_e32 v[8:9], s[14:15]
	v_mov_b64_e32 v[10:11], s[16:17]
	v_mov_b64_e32 v[12:13], s[18:19]
	v_mov_b64_e32 v[14:15], s[20:21]
	s_waitcnt lgkmcnt(0)
	v_mfma_f32_32x32x16_bf16 v[18:33], v[50:53], v[142:145], v[18:33]
	s_nop 2
	v_max_f32_e32 v50, v35, v35
	v_max_f32_e32 v51, v34, v34
	v_max_f32_e32 v50, v51, v50
	v_max3_f32 v50, v50, v36, v37
	v_max3_f32 v50, v50, v38, v39
	v_max3_f32 v50, v50, v40, v41
	v_max3_f32 v50, v50, v42, v43
	v_max3_f32 v50, v50, v44, v45
	v_max3_f32 v50, v50, v46, v47
	v_max3_f32 v50, v50, v48, v49
	v_max3_f32 v50, v50, v18, v19
	v_max3_f32 v50, v50, v20, v21
	v_max3_f32 v50, v50, v22, v23
	v_max3_f32 v50, v50, v24, v25
	v_max3_f32 v50, v50, v26, v27
	v_max3_f32 v50, v50, v28, v29
	v_max3_f32 v50, v50, v30, v31
	v_max3_f32 v50, v50, v32, v33
	v_mov_b32_e32 v51, v50
	s_nop 1
	v_permlane32_swap_b32_e32 v50, v51
	v_max_f32_e32 v51, v51, v51
	v_max_f32_e32 v50, v50, v50
	v_max_f32_e32 v204, v50, v51
	v_sub_f32_e32 v34, v34, v204
	v_exp_f32_e32 v50, v34
	v_sub_f32_e32 v34, v35, v204
	v_exp_f32_e32 v51, v34
	v_sub_f32_e32 v34, v36, v204
	v_exp_f32_e32 v52, v34
	v_sub_f32_e32 v34, v37, v204
	v_exp_f32_e32 v53, v34
	v_sub_f32_e32 v34, v38, v204
	v_exp_f32_e32 v54, v34
	v_sub_f32_e32 v34, v39, v204
	v_exp_f32_e32 v55, v34
	v_sub_f32_e32 v34, v40, v204
	v_exp_f32_e32 v56, v34
	v_sub_f32_e32 v34, v41, v204
	v_exp_f32_e32 v57, v34
	v_sub_f32_e32 v34, v42, v204
	v_mov_b64_e32 v[16:17], s[22:23]
	v_exp_f32_e32 v58, v34
	v_sub_f32_e32 v34, v43, v204
	v_sub_f32_e32 v67, v19, v204
	s_add_i32 s8, s53, 0
	v_bfe_u32 v19, v86, 1, 5
	v_exp_f32_e32 v59, v34
	v_sub_f32_e32 v34, v44, v204
	v_sub_f32_e32 v68, v20, v204
	s_add_i32 s8, s8, 0x1e800
	v_and_b32_e32 v20, 28, v19
	s_or_b32 s10, s52, s2
	v_exp_f32_e32 v60, v34
	v_sub_f32_e32 v34, v45, v204
	v_sub_f32_e32 v69, v21, v204
	v_add_u32_e32 v201, s8, v20
	v_mov_b32_e32 v21, s8
	s_lshl_b32 s8, s54, 10
	s_ashr_i32 s11, s10, 31
	v_exp_f32_e32 v61, v34
	v_sub_f32_e32 v34, v46, v204
	s_add_i32 s89, s8, 0xf7f80000
	s_lshl_b64 s[12:13], s[10:11], 19
	v_exp_f32_e32 v62, v34
	v_sub_f32_e32 v34, v47, v204
	v_sub_f32_e32 v66, v18, v204
	v_lshrrev_b32_e32 v18, 2, v86
	s_add_u32 s12, s50, s12
	v_exp_f32_e32 v63, v34
	v_sub_f32_e32 v34, v48, v204
	v_sub_f32_e32 v70, v22, v204
	v_and_b32_e32 v128, 14, v18
	v_lshrrev_b32_e32 v22, 3, v86
	v_and_b32_e32 v18, 12, v18
	s_addc_u32 s13, s51, s13
	s_mul_i32 s8, s10, 0xc0000
	v_exp_f32_e32 v64, v34
	v_sub_f32_e32 v34, v49, v204
	v_mad_u32_u24 v199, v19, s78, v21
	v_and_b32_e32 v19, 0x80, v92
	v_and_b32_e32 v21, 16, v94
	v_and_b32_e32 v22, 4, v22
	v_and_or_b32 v198, v93, s77, v18
	v_or_b32_e32 v18, s61, v87
	s_mul_hi_i32 s2, s10, 0xc0000
	s_add_u32 s6, s6, s8
	v_exp_f32_e32 v65, v34
	v_or3_b32 v197, v19, v22, v21
	v_or3_b32 v18, v18, v88, v89
	v_mov_b32_e32 v19, v175
	s_addc_u32 s2, s7, s2
	v_and_b32_e32 v20, 1, v86

; #define C_SPLAT() do { _Pragma("unroll") for (int _r = 0; _r < 16; ++_r) cinit[_r] = -m_reg; asm volatile("" : "+v"(cinit)); } while (0)
; template <bool FIRST> DEVI bool partialSM(f32x16& p0, f32x16& p1, float& m_reg, float& alpha) {
;     ...
;     if (FIRST) { m_reg = pmax; alpha = 1.f;
; #pragma unroll
;         for (int r = 0; r < 16; ++r) { p0[r] = __builtin_amdgcn_exp2f(p0[r] - pmax); p1[r] = p1[r] - pmax; }
;         return false;
; DEVI void attn_unit8(const Params& p, char* smem, int unit, int l, int& cvs  , CvRun& crun) {
;     ...
;     { f32x16 z; _Pragma("unroll") for (int r = 0; r < 16; ++r) z[r] = 0.f;
;       qkt(pA0, pA1, K_lds, qr, r32, hi, z); } partialSM<true>(pA0, pA1, m_reg, alA); C_SPLAT();
;     int s0 = 0, s1 = 1, s2 = 2;
	s_add_u32 s6, s6, 0xc000
	v_xor_b32_e32 v34, 0x80000000, v204
	v_sub_f32_e32 v81, v33, v204
	v_sub_f32_e32 v80, v32, v204
	v_sub_f32_e32 v79, v31, v204
	v_sub_f32_e32 v78, v30, v204
	v_sub_f32_e32 v77, v29, v204
	v_sub_f32_e32 v76, v28, v204
	v_sub_f32_e32 v75, v27, v204
	v_sub_f32_e32 v74, v26, v204
	v_sub_f32_e32 v73, v25, v204
	v_sub_f32_e32 v72, v24, v204
	v_sub_f32_e32 v71, v23, v204
	v_lshlrev_b32_e32 v200, 5, v20
	v_lshlrev_b32_e32 v180, 4, v20
	v_mov_b32_e32 v116, v18
	v_add_u32_e32 v117, 0x2000, v18
	s_addc_u32 s7, s2, 0
	s_add_u32 s44, s12, 0x8000
	s_addc_u32 s45, s13, 0
	v_mov_b64_e32 v[32:33], v[16:17]
	v_mov_b32_e32 v35, v34
	v_mov_b32_e32 v36, v34
	v_mov_b32_e32 v37, v34
	v_mov_b32_e32 v38, v34
	v_mov_b32_e32 v39, v34
	v_mov_b32_e32 v40, v34
	v_mov_b32_e32 v41, v34
	v_mov_b32_e32 v42, v34
	v_mov_b32_e32 v43, v34
	v_mov_b32_e32 v44, v34
	v_mov_b32_e32 v45, v34
	v_mov_b32_e32 v46, v34
	v_mov_b32_e32 v47, v34
	v_mov_b32_e32 v48, v34
	v_mov_b32_e32 v49, v34
	v_mov_b32_e32 v118, v174
	v_mov_b32_e32 v120, v82
	v_mov_b32_e32 v122, v84
	s_mov_b64 s[12:13], s[6:7]
	s_add_u32 s67, s6, 0xb4000
	v_mov_b64_e32 v[30:31], v[14:15]
	v_mov_b64_e32 v[28:29], v[12:13]
	v_mov_b64_e32 v[26:27], v[10:11]
	v_mov_b64_e32 v[24:25], v[8:9]
	v_mov_b64_e32 v[22:23], v[6:7]
	v_mov_b64_e32 v[20:21], v[4:5]
	v_mov_b64_e32 v[18:19], v[2:3]
	s_mov_b32 s6, 2
	s_mov_b32 s61, 1

; DEVI f32x4 ld_nt(const float* p) { return __builtin_nontemporal_load((const f32x4*)p); }
; DEVI void cv_next(const Params& p, int l, int s, int lane, int stride, CvRun& run) {
;     ...
;     run.c = cv_slice(p, l, s, lane); run.left = 0;
;     if ((stride & 511) == 0) {
;         if (s < NS_W13) { const int e = s >> 9, es = stride >> 9; if (e < NE) { run.left = (NE - 1 - e) / es; run.sstep = (long)es * 1024 * 256; run.dstep = (long)es * 512 * 1024; } }
;         else { const int e = (s - NS_W13) >> 8, es = stride >> 8; if (e < NE) { run.left = (NE - 1 - e) / es; run.sstep = (long)es * 256 * 1024; run.dstep = (long)es * 1024 * 256; } } }
; }
; DEVI void cv_issue(const Params& p, int l, int s, int lane, CvRegs& R, CvRun& run) {
;     R.live = s < NS_SLICES ? 1 : 0;
;     if (R.live) { cv_next(p, l, s, lane, (int)gridDim.x * 8, run); R.c = run.c; const int kq = lane >> 3;
;         const float* sp = R.c.src + (size_t)(R.c.k0 + 2 * kq) * R.c.ld;
;         R.a0 = ld_nt(sp); R.b0 = ld_nt(sp + R.c.ld); R.a1 = ld_nt(sp + (size_t)16 * R.c.ld); R.b1 = ld_nt(sp + (size_t)17 * R.c.ld); }
.LBB0_2259:
	v_add_u32_e32 v252, s10, v128
	s_mov_b64 s[68:69], s[18:19]
	s_mov_b64 s[40:41], s[20:21]
	v_mul_lo_u32 v243, v252, s6
	v_lshlrev_b32_e32 v242, 2, v114
	s_lshl_b32 s72, s6, 2
	s_lshl_b32 s73, s6, 6
	v_lshl_add_u32 v242, v243, 2, v242
	v_add_u32_e32 v243, s72, v242
	v_add_u32_e32 v244, s73, v242
	v_add_u32_e32 v245, s73, v243
	s_cmp_eq_u32 s95, 0
	s_cselect_b64 s[72:73], -1, 0
	v_cndmask_b32_e64 v246, v197, v198, s[72:73]
	v_or_b32_e32 v246, v246, v196
	v_add_u32_e32 v246, s8, v246
	v_mul_lo_u32 v246, v246, s94
	v_add3_u32 v246, v246, v180, s10
	v_lshlrev_b32_e32 v246, 1, v246
	v_mov_b32_e32 v247, 0
	s_ashr_i32 s7, s6, 31
	v_mad_i64_i32 v[252:253], s[16:17], v252, s6, 0
	v_lshl_add_u64 v[252:253], v[252:253], 2, v[250:251]
	s_lshl_b64 s[16:17], s[6:7], 2
	v_lshl_add_u64 v[254:255], v[252:253], 0, s[16:17]
	global_load_dwordx4 v[154:157], v[252:253], off nt
	global_load_dwordx4 v[158:161], v[254:255], off nt
	v_mad_i64_i32 v[252:253], s[18:19], s6, 60, v[254:255]
	v_lshl_add_u64 v[254:255], v[252:253], 0, s[16:17]
	global_load_dwordx4 v[162:165], v[252:253], off nt
	global_load_dwordx4 v[166:169], v[254:255], off nt
	s_mov_b64 s[26:27], s[22:23]
	s_mov_b64 s[28:29], s[50:51]
	s_mov_b32 s56, s11
	s_mov_b32 s55, s95
	v_mov_b64_e32 v[170:171], v[250:251]
	s_mov_b32 s57, s6
	s_mov_b32 s58, s10
	v_mov_b64_e32 v[172:173], v[182:183]
	s_mov_b32 s59, s94
	s_mov_b32 s60, s8

; DEVI void attn_unit8(const Params& p, char* smem, int unit, int l, int& cvs  , CvRun& crun) {
;     ...
;     for (int T = 0; T + 1 < NTILE; ++T) {
;         const char* Kb = K_lds + s0 * 24576; const int vb = vb0 + s0 * 16384;
;     ...
;         if (T + 2 < NTILE) B_DMA(T + 2, s2);
.LBB0_2266:
	s_mul_i32 s98, s61, 0x6000
	s_add_i32 s98, s96, s98
	s_lshl_b32 s99, s61, 14
	s_add_i32 s99, s97, s99
	s_mul_i32 s6, s2, 0x6000
	s_add_i32 s6, s6, 0
	v_add_u32_e32 v249, s6, v129

; DEVI void qkt(f32x16& p0, f32x16& p1, const char* Kb, const bf16x8 (&qr)[6], int r32, int hi, const f32x16& cinit) {
; #pragma unroll
;     for (int d0 = 0; d0 < 6; ++d0) { const int cb = (d0 * 16 + hi * 8) * 2;
;         const bf16x8 k0 = *(const bf16x8*)(Kb + KSWZ(r32, cb)), k1 = *(const bf16x8*)(Kb + KSWZ(32 + r32, cb));
;         p0 = __builtin_amdgcn_mfma_f32_32x32x16_bf16(k0, qr[d0], d0 == 0 ? cinit : p0, 0, 0, 0);
;         p1 = __builtin_amdgcn_mfma_f32_32x32x16_bf16(k1, qr[d0], d0 == 0 ? cinit : p1, 0, 0, 0); }
; }
	s_mov_b32 m0, s98
	s_barrier
	ds_read_b128 v[234:237], v249
	ds_read_b128 v[212:215], v249 offset:6144
	global_load_lds_dwordx4 v118, s[12:13]
	s_waitcnt lgkmcnt(1)
	v_mfma_f32_32x32x16_bf16 v[98:113], v[234:237], v[150:153], v[34:49]
	s_add_i32 m0, s98, 0x2000

; DEVI void qkt(f32x16& p0, f32x16& p1, const char* Kb, const bf16x8 (&qr)[6], int r32, int hi, const f32x16& cinit) {
; #pragma unroll
;     for (int d0 = 0; d0 < 6; ++d0) { const int cb = (d0 * 16 + hi * 8) * 2;
;         const bf16x8 k0 = *(const bf16x8*)(Kb + KSWZ(r32, cb)), k1 = *(const bf16x8*)(Kb + KSWZ(32 + r32, cb));
;         p0 = __builtin_amdgcn_mfma_f32_32x32x16_bf16(k0, qr[d0], d0 == 0 ? cinit : p0, 0, 0, 0);
;         p1 = __builtin_amdgcn_mfma_f32_32x32x16_bf16(k1, qr[d0], d0 == 0 ? cinit : p1, 0, 0, 0); }
; }
	v_add_u32_e32 v126, s6, v184
	global_load_lds_dwordx4 v120, s[12:13]
	s_waitcnt lgkmcnt(0)
	v_mfma_f32_32x32x16_bf16 v[66:81], v[212:215], v[150:153], v[34:49]
	ds_read_b128 v[212:215], v126
	ds_read_b128 v[216:219], v126 offset:6144
	s_add_i32 m0, s98, 0x4000

; DEVI void qkt(f32x16& p0, f32x16& p1, const char* Kb, const bf16x8 (&qr)[6], int r32, int hi, const f32x16& cinit) {
; #pragma unroll
;     for (int d0 = 0; d0 < 6; ++d0) { const int cb = (d0 * 16 + hi * 8) * 2;
;         const bf16x8 k0 = *(const bf16x8*)(Kb + KSWZ(r32, cb)), k1 = *(const bf16x8*)(Kb + KSWZ(32 + r32, cb));
;         p0 = __builtin_amdgcn_mfma_f32_32x32x16_bf16(k0, qr[d0], d0 == 0 ? cinit : p0, 0, 0, 0);
;         p1 = __builtin_amdgcn_mfma_f32_32x32x16_bf16(k1, qr[d0], d0 == 0 ? cinit : p1, 0, 0, 0); }
; }
	v_add_u32_e32 v126, s6, v185
	global_load_lds_dwordx4 v122, s[12:13]
	s_waitcnt lgkmcnt(1)
	v_mfma_f32_32x32x16_bf16 v[98:113], v[212:215], v[138:141], v[98:113]
	s_mov_b32 m0, s99
	s_nop 0
	global_load_lds_dwordx4 v116, s[44:45]
	s_add_i32 m0, s99, 0x2000


; template <int OFF> DEVI s16x4 tr_read(int vb) { s16x4 r; asm volatile("ds_read_b64_tr_b16 %0, %1 offset:%2" : "=&v"(r) : "v"(vb), "i"(OFF) : "memory"); return r; }
; #define SBAR() __builtin_amdgcn_sched_barrier(0)
; #define PK4(P, BASE, OUT) do { u32x4 w = {cvt_pk_bf16(P[BASE + 0], P[BASE + 1]), cvt_pk_bf16(P[BASE + 2], P[BASE + 3]), cvt_pk_bf16(P[BASE + 4], P[BASE + 5]), cvt_pk_bf16(P[BASE + 6], P[BASE + 7])}; \
;     OUT = *reinterpret_cast<bf16x8*>(&w); } while (0)
; DEVI void pv_both(f32x16& o0, f32x16& o1, int vb, bf16x8 pa0, bf16x8 pa1, bf16x8 pa2, bf16x8 pa3) {
;     const s16x4 a0 = tr_read<v_rd_off(0, 0, 0)>(vb), b0 = tr_read<v_rd_off(0, 0, 1)>(vb), a1 = tr_read<v_rd_off(0, 1, 0)>(vb), b1 = tr_read<v_rd_off(0, 1, 1)>(vb);
;     const s16x4 a2 = tr_read<v_rd_off(0, 2, 0)>(vb), b2 = tr_read<v_rd_off(0, 2, 1)>(vb), a3 = tr_read<v_rd_off(0, 3, 0)>(vb), b3 = tr_read<v_rd_off(0, 3, 1)>(vb);
;     const s16x4 c0 = tr_read<v_rd_off(1, 0, 0)>(vb), d0 = tr_read<v_rd_off(1, 0, 1)>(vb), c1 = tr_read<v_rd_off(1, 1, 0)>(vb), d1 = tr_read<v_rd_off(1, 1, 1)>(vb);
;     const s16x4 c2 = tr_read<v_rd_off(1, 2, 0)>(vb), d2 = tr_read<v_rd_off(1, 2, 1)>(vb), c3 = tr_read<v_rd_off(1, 3, 0)>(vb), d3 = tr_read<v_rd_off(1, 3, 1)>(vb);
;     asm volatile("s_waitcnt lgkmcnt(8)" ::: "memory"); SBAR();
; DEVI void finishSM(f32x16& p0, f32x16& p1, float alpha, float& l_reg, bf16x8& pa0, bf16x8& pa1, bf16x8& pa2, bf16x8& pa3) {
; #pragma unroll
;     for (int r = 0; r < 16; ++r) p1[r] = __builtin_amdgcn_exp2f(p1[r]);
;     f32x2 s2 = (f32x2){p0[0], p0[1]} + (f32x2){p1[0], p1[1]};
; #pragma unroll
;     for (int r = 2; r < 16; r += 2) s2 += (f32x2){p0[r], p0[r + 1]} + (f32x2){p1[r], p1[r + 1]};
;     float ps = s2[0] + s2[1];
;     { auto rr = __builtin_amdgcn_permlane32_swap(__float_as_uint(ps), __float_as_uint(ps), false, false);
;       ps = __uint_as_float(rr[0]) + __uint_as_float(rr[1]); }
;     l_reg = l_reg * alpha + ps;
;     ...
;     PK4(p0, 0, pa0); PK4(p0, 8, pa1); PK4(p1, 0, pa2); PK4(p1, 8, pa3);
;     ...
; }
	s_waitcnt lgkmcnt(0)
	v_mfma_f32_32x32x16_bf16 v[66:81], v[216:219], v[138:141], v[66:81]
	global_load_lds_dwordx4 v117, s[44:45]
	ds_read_b128 v[212:215], v126
	ds_read_b128 v[216:219], v126 offset:6144
	v_add_u32_e32 v126, s6, v205
	s_waitcnt lgkmcnt(1)
	v_mfma_f32_32x32x16_bf16 v[98:113], v[212:215], v[134:137], v[98:113]
	ds_read_b128 v[212:215], v126
	ds_read_b128 v[220:223], v126 offset:6144
	v_add_u32_e32 v126, s6, v206
	s_waitcnt lgkmcnt(2)
	v_mfma_f32_32x32x16_bf16 v[66:81], v[216:219], v[134:137], v[66:81]
	ds_read_b128 v[216:219], v126
	ds_read_b128 v[224:227], v126 offset:6144
	v_add_u32_e32 v126, s6, v207
	ds_read_b128 v[228:231], v126
	ds_read_b128 v[232:235], v126 offset:6144
	v_add_f32_e32 v126, v50, v82
	v_add_f32_e32 v127, v51, v83
	v_cvt_pk_bf16_f32 v50, v50, v51
	v_cvt_pk_bf16_f32 v51, v52, v53
	s_waitcnt lgkmcnt(5)
	v_mfma_f32_32x32x16_bf16 v[98:113], v[212:215], v[130:133], v[98:113]
	v_add_f32_e64 v212, v52, v84
	v_add_f32_e64 v213, v53, v85
	v_cvt_pk_bf16_f32 v52, v54, v55
	v_cvt_pk_bf16_f32 v53, v56, v57
	v_add_f32_e64 v126, v212, v126
	v_add_f32_e64 v127, v213, v127
	v_add_f32_e64 v212, v54, v86
	v_add_f32_e64 v213, v55, v87
	v_cvt_pk_bf16_f32 v54, v58, v59
	s_waitcnt lgkmcnt(4)
	v_mfma_f32_32x32x16_bf16 v[66:81], v[220:223], v[130:133], v[66:81]
	v_add_f32_e64 v126, v212, v126
	v_add_f32_e64 v127, v213, v127
	v_add_f32_e64 v212, v56, v88
	v_add_f32_e64 v213, v57, v89
	v_cvt_pk_bf16_f32 v55, v60, v61
	v_cvt_pk_bf16_f32 v56, v62, v63
	v_cvt_pk_bf16_f32 v57, v64, v65
	v_add_f32_e64 v126, v212, v126
	v_add_f32_e64 v127, v213, v127
	v_add_f32_e32 v212, v58, v90
	v_add_f32_e32 v213, v59, v91
	v_cvt_pk_bf16_f32 v58, v82, v83
	v_cvt_pk_bf16_f32 v59, v84, v85
	s_waitcnt lgkmcnt(3)
	v_mfma_f32_32x32x16_bf16 v[98:113], v[216:219], v[146:149], v[98:113]
	v_add_f32_e64 v126, v212, v126
	v_add_f32_e64 v127, v213, v127
	v_add_f32_e64 v212, v60, v92
	v_add_f32_e64 v213, v61, v93
	v_cvt_pk_bf16_f32 v60, v86, v87
	v_cvt_pk_bf16_f32 v61, v88, v89
	v_add_f32_e64 v126, v212, v126
	v_add_f32_e64 v127, v213, v127
	v_add_f32_e32 v212, v62, v94
	v_add_f32_e32 v213, v63, v95
	v_cvt_pk_bf16_f32 v62, v90, v91
	v_cvt_pk_bf16_f32 v63, v92, v93
	s_waitcnt lgkmcnt(2)
	v_mfma_f32_32x32x16_bf16 v[66:81], v[224:227], v[146:149], v[66:81]
	v_add_f32_e64 v126, v212, v126
	v_add_f32_e64 v127, v213, v127
	v_add_f32_e64 v212, v64, v96
	v_add_f32_e64 v213, v65, v97
	v_cvt_pk_bf16_f32 v64, v94, v95
	v_cvt_pk_bf16_f32 v65, v96, v97
	ds_read_b64_tr_b16 v[154:155], v203 offset:0x2000
	ds_read_b64_tr_b16 v[156:157], v203 offset:0x2400
	ds_read_b64_tr_b16 v[158:159], v203 offset:0x2800
	ds_read_b64_tr_b16 v[160:161], v203 offset:0x2c00
	ds_read_b64_tr_b16 v[162:163], v203 offset:0x3000
	ds_read_b64_tr_b16 v[164:165], v203 offset:0x3400
	ds_read_b64_tr_b16 v[166:167], v203 offset:0x3800
	ds_read_b64_tr_b16 v[168:169], v203 offset:0x3c00
	v_add_f32_e64 v126, v212, v126
	v_add_f32_e64 v127, v213, v127
	ds_read_b64_tr_b16 v[212:213], v203 offset:0x2200
	ds_read_b64_tr_b16 v[214:215], v203 offset:0x2600
	ds_read_b64_tr_b16 v[216:217], v203 offset:0x2a00
	s_waitcnt lgkmcnt(12)
	v_mfma_f32_32x32x16_bf16 v[98:113], v[228:231], v[142:145], v[98:113]
	ds_read_b64_tr_b16 v[218:219], v203 offset:0x2e00
	ds_read_b64_tr_b16 v[220:221], v203 offset:0x3200
	ds_read_b64_tr_b16 v[222:223], v203 offset:0x3600
	ds_read_b64_tr_b16 v[224:225], v203 offset:0x3a00
	ds_read_b64_tr_b16 v[226:227], v203 offset:0x3e00
	v_add_f32_e32 v126, v126, v127
	s_waitcnt lgkmcnt(15)
	v_mfma_f32_32x32x16_bf16 v[66:81], v[232:235], v[142:145], v[66:81]
	v_mov_b32_e32 v127, v126


; #define SBAR() __builtin_amdgcn_sched_barrier(0)
; DEVI void pv_both(f32x16& o0, f32x16& o1, int vb, bf16x8 pa0, bf16x8 pa1, bf16x8 pa2, bf16x8 pa3) {
;     ...
;     o0 = __builtin_amdgcn_mfma_f32_32x32x16_bf16(pa0, PK(a0, b0), o0, 0, 0, 0);
;     o0 = __builtin_amdgcn_mfma_f32_32x32x16_bf16(pa1, PK(a1, b1), o0, 0, 0, 0);
;     o0 = __builtin_amdgcn_mfma_f32_32x32x16_bf16(pa2, PK(a2, b2), o0, 0, 0, 0);
;     o0 = __builtin_amdgcn_mfma_f32_32x32x16_bf16(pa3, PK(a3, b3), o0, 0, 0, 0);
;     asm volatile("s_waitcnt lgkmcnt(0)" ::: "memory"); SBAR();
;     o1 = __builtin_amdgcn_mfma_f32_32x32x16_bf16(pa0, PK(c0, d0), o1, 0, 0, 0);
;     o1 = __builtin_amdgcn_mfma_f32_32x32x16_bf16(pa1, PK(c1, d1), o1, 0, 0, 0);
;     o1 = __builtin_amdgcn_mfma_f32_32x32x16_bf16(pa2, PK(c2, d2), o1, 0, 0, 0);
;     o1 = __builtin_amdgcn_mfma_f32_32x32x16_bf16(pa3, PK(c3, d3), o1, 0, 0, 0);
;     ...
; }
; template <bool FIRST> DEVI bool partialSM(f32x16& p0, f32x16& p1, float& m_reg, float& alpha) {
;     float pmax = p0[0];
; #pragma unroll
;     for (int r = 1; r < 16; ++r) pmax = fmaxf(pmax, p0[r]);
; #pragma unroll
;     for (int r = 0; r < 16; ++r) pmax = fmaxf(pmax, p1[r]);
;     { auto rr = __builtin_amdgcn_permlane32_swap(__float_as_uint(pmax), __float_as_uint(pmax), false, false);
;       pmax = fmaxf(__uint_as_float(rr[0]), __uint_as_float(rr[1])); }
	s_waitcnt lgkmcnt(14)
	v_mfma_f32_32x32x16_bf16 v[18:33], v[50:53], v[154:157], v[18:33]
	v_permlane32_swap_b32_e32 v126, v127
	s_waitcnt lgkmcnt(6)
	v_mfma_f32_32x32x16_bf16 v[2:17], v[50:53], v[212:215], v[2:17]
	s_nop 1
	v_max_f32_e32 v249, v99, v99
	v_max_f32_e32 v250, v98, v98
	v_max_f32_e32 v249, v250, v249
	v_max3_f32 v249, v249, v100, v101
	v_max3_f32 v249, v249, v102, v103
	v_max3_f32 v251, v249, v104, v105
	v_max3_f32 v251, v251, v106, v107
	v_exp_f32_e32 v50, v98
	v_exp_f32_e32 v51, v99
	v_exp_f32_e32 v52, v100
	v_exp_f32_e32 v53, v101
	v_mfma_f32_32x32x16_bf16 v[18:33], v[54:57], v[158:161], v[18:33]
	s_waitcnt lgkmcnt(4)
	v_mfma_f32_32x32x16_bf16 v[2:17], v[54:57], v[216:219], v[2:17]
	v_max3_f32 v251, v251, v108, v109
	v_max3_f32 v251, v251, v110, v111
	v_max3_f32 v251, v251, v112, v113
	v_max3_f32 v251, v251, v66, v67
	v_max3_f32 v251, v251, v68, v69
	v_max3_f32 v251, v251, v70, v71
	v_max3_f32 v251, v251, v72, v73
	v_exp_f32_e32 v54, v102
	v_exp_f32_e32 v55, v103
	v_exp_f32_e32 v56, v104
	v_exp_f32_e32 v57, v105
	v_mfma_f32_32x32x16_bf16 v[18:33], v[58:61], v[162:165], v[18:33]
	s_waitcnt lgkmcnt(2)
	v_mfma_f32_32x32x16_bf16 v[2:17], v[58:61], v[220:223], v[2:17]
	v_max3_f32 v251, v251, v74, v75
	v_max3_f32 v251, v251, v76, v77
	v_max3_f32 v251, v251, v78, v79
	v_max3_f32 v251, v251, v80, v81
	v_mov_b32_e32 v252, v251


; #define SBAR() __builtin_amdgcn_sched_barrier(0)
; DEVI void pv_both(f32x16& o0, f32x16& o1, int vb, bf16x8 pa0, bf16x8 pa1, bf16x8 pa2, bf16x8 pa3) {
;     ...
;     asm volatile("s_waitcnt lgkmcnt(0)" ::: "memory"); SBAR();
;     o1 = __builtin_amdgcn_mfma_f32_32x32x16_bf16(pa0, PK(c0, d0), o1, 0, 0, 0);
;     o1 = __builtin_amdgcn_mfma_f32_32x32x16_bf16(pa1, PK(c1, d1), o1, 0, 0, 0);
;     o1 = __builtin_amdgcn_mfma_f32_32x32x16_bf16(pa2, PK(c2, d2), o1, 0, 0, 0);
;     o1 = __builtin_amdgcn_mfma_f32_32x32x16_bf16(pa3, PK(c3, d3), o1, 0, 0, 0);
;     ...
; }
; template <bool FIRST> DEVI bool partialSM(f32x16& p0, f32x16& p1, float& m_reg, float& alpha) {
;     float pmax = p0[0];
; #pragma unroll
;     for (int r = 1; r < 16; ++r) pmax = fmaxf(pmax, p0[r]);
; #pragma unroll
;     for (int r = 0; r < 16; ++r) pmax = fmaxf(pmax, p1[r]);
;     { auto rr = __builtin_amdgcn_permlane32_swap(__float_as_uint(pmax), __float_as_uint(pmax), false, false);
;       pmax = fmaxf(__uint_as_float(rr[0]), __uint_as_float(rr[1])); }
;     if (FIRST) { m_reg = pmax; alpha = 1.f;
; #pragma unroll
;         for (int r = 0; r < 16; ++r) { p0[r] = __builtin_amdgcn_exp2f(p0[r] - pmax); p1[r] = p1[r] - pmax; }
;         return false;
;     } else if (__builtin_expect(__all(pmax <= ATT_THR), 1)) { alpha = 1.f;
; #pragma unroll
;         for (int r = 0; r < 16; ++r) p0[r] = __builtin_amdgcn_exp2f(p0[r]);
;         return false;
	v_exp_f32_e32 v58, v106
	v_exp_f32_e32 v59, v107
	v_permlane32_swap_b32_e32 v251, v252
	v_exp_f32_e32 v60, v108
	v_exp_f32_e32 v61, v109
	v_mfma_f32_32x32x16_bf16 v[18:33], v[62:65], v[166:169], v[18:33]
	s_waitcnt lgkmcnt(0)
	v_mfma_f32_32x32x16_bf16 v[2:17], v[62:65], v[224:227], v[2:17]
	v_exp_f32_e32 v62, v110
	v_exp_f32_e32 v63, v111
	v_exp_f32_e32 v64, v112
	v_exp_f32_e32 v65, v113
	v_max_f32_e32 v252, v252, v252
	v_max_f32_e32 v251, v251, v251
	v_max_f32_e32 v174, v251, v252
	v_cmp_ge_f32_e32 vcc, s80, v174
	s_cmp_lg_u64 vcc, exec
	s_cselect_b64 s[6:7], -1, 0
	s_cbranch_scc1 .LBB0_2275
	v_mov_b32_e32 v203, 1.0
	v_mov_b32_e32 v204, v210
	s_branch .LBB0_2280

; DEVI f32x4 ld_nt(const float* p) { return __builtin_nontemporal_load((const f32x4*)p); }
; DEVI void cv_next(const Params& p, int l, int s, int lane, int stride, CvRun& run) {
;     ...
;     run.c = cv_slice(p, l, s, lane); run.left = 0;
;     if ((stride & 511) == 0) {
;         if (s < NS_W13) { const int e = s >> 9, es = stride >> 9; if (e < NE) { run.left = (NE - 1 - e) / es; run.sstep = (long)es * 1024 * 256; run.dstep = (long)es * 512 * 1024; } }
;         else { const int e = (s - NS_W13) >> 8, es = stride >> 8; if (e < NE) { run.left = (NE - 1 - e) / es; run.sstep = (long)es * 256 * 1024; run.dstep = (long)es * 1024 * 256; } } }
; }
; DEVI void cv_issue(const Params& p, int l, int s, int lane, CvRegs& R, CvRun& run) {
;     R.live = s < NS_SLICES ? 1 : 0;
;     if (R.live) { cv_next(p, l, s, lane, (int)gridDim.x * 8, run); R.c = run.c; const int kq = lane >> 3;
;         const float* sp = R.c.src + (size_t)(R.c.k0 + 2 * kq) * R.c.ld;
;         R.a0 = ld_nt(sp); R.b0 = ld_nt(sp + R.c.ld); R.a1 = ld_nt(sp + (size_t)16 * R.c.ld); R.b1 = ld_nt(sp + (size_t)17 * R.c.ld); }
.LBB0_2282:
	v_mov_b32_e32 v172, s40
	v_mov_b32_e32 v173, s41
	s_mov_b64 s[44:45], 0x4000
	v_lshlrev_b32_e32 v250, 2, v114
	v_mov_b32_e32 v251, 0
	v_lshl_add_u64 v[170:171], s[68:69], 0, v[250:251]
	s_cmp_lt_i32 s54, 0x30300
	s_cselect_b64 s[12:13], -1, 0
	s_cmp_gt_i32 s54, 0x302ff
	s_cbranch_scc1 .LBB0_2312
	s_cmp_gt_i32 s56, 0
	s_mov_b64 s[14:15], -1
	s_cbranch_scc1 .LBB0_2309
	s_cmp_gt_i32 s54, 0x201ff
	s_cselect_b64 s[14:15], -1, 0
	s_cmp_lt_i32 s54, 0x20200
	s_mov_b64 s[6:7], -1
	s_cbranch_scc1 .LBB0_2286
	s_add_i32 s2, s54, 0xfffdfe00
	s_lshr_b32 s8, s2, 8
	s_and_b32 s10, s54, 0xe0
	s_cmp_lt_u32 s2, 0x10000
	s_cselect_b64 s[6:7], -1, 0
	s_lshl_b32 s2, s2, 10
	s_and_b32 s2, s2, 0x3fc0000
	s_bitset1_b32 s2, 26
	s_and_b64 s[6:7], s[6:7], exec
	s_cselect_b32 s6, 0xc0, s79
	s_cselect_b32 s2, s2, 0x40000
	s_add_u32 s6, s24, s6
	s_addc_u32 s7, s25, 0
	s_load_dwordx2 s[6:7], s[6:7], 0x0
	s_lshl_b32 s2, s2, 2
	s_load_dwordx2 s[18:19], s[24:25], 0x158
	s_waitcnt lgkmcnt(0)
	s_add_u32 s2, s6, s2
	s_addc_u32 s6, s7, 0
	s_lshl_b32 s7, s54, 7
	s_lshl_b32 s11, s54, 5
	s_and_b32 s7, s7, 0xf80
	s_add_u32 s16, s2, s7
	s_addc_u32 s17, s6, 0
	s_lshl_b64 s[6:7], s[8:9], 19
	s_add_u32 s18, s18, s6
	s_addc_u32 s19, s19, s7
	s_lshl_b32 s6, s54, 4
	s_and_b32 s2, s11, 0x300
	s_and_b32 s6, s6, 0x60
	s_or_b32 s2, s2, s6
	s_lshl_b32 s6, s54, 3
	s_and_b32 s6, s6, 8
	s_or_b32 s8, s2, s6
	s_mov_b64 s[6:7], 0
